# v49 + hand-written two-candidate near-tie path (rows loaded up front, five fp64 wave reductions interleaved); other counts use the compiled loop
# baseline (speedup 1.0000x reference)
.LBB0_118:
	s_waitcnt vmcnt(0)
	v_lshrrev_b32_e32 v67, 4, v0
	v_mov_b32_e32 v66, 0x11100
	v_lshl_or_b32 v66, v67, 2, v66
	s_waitcnt lgkmcnt(0)
	s_barrier
	ds_read_b32 v66, v66
	v_mul_u32_u24_e32 v68, 0x102, v67
	v_lshlrev_b32_e32 v72, 3, v68
	s_waitcnt lgkmcnt(0)
	v_max_i32_e32 v66, 1, v66
	v_cvt_f32_u32_e32 v66, v66
	v_div_scale_f32 v69, s[0:1], v66, v66, 1.0
	v_rcp_f32_e32 v70, v69
	v_div_scale_f32 v68, vcc, 1.0, v66, 1.0
	v_fma_f32 v71, -v69, v70, 1.0
	v_fmac_f32_e32 v70, v71, v70
	v_mul_f32_e32 v71, v68, v70
	v_fma_f32 v73, -v69, v71, v68
	v_fmac_f32_e32 v71, v73, v70
	v_fma_f32 v68, -v69, v71, v68
	v_div_fmas_f32 v73, v68, v70, v71
	v_lshl_add_u32 v68, v138, 3, v72
	v_add_u32_e32 v76, 0x8000, v68
	ds_read2_b64 v[68:71], v76 offset1:16
	v_div_fixup_f32 v77, v73, v66, 1.0
	v_mul_i32_i24_e32 v73, 0xfffffbf8, v67
	v_lshlrev_b32_e32 v66, 2, v138
	v_add3_u32 v78, v72, v73, v66
	ds_read2_b64 v[72:75], v76 offset0:32 offset1:48
	s_waitcnt lgkmcnt(1)
	v_cvt_f32_f64_e32 v68, v[68:69]
	v_cvt_f32_f64_e32 v69, v[70:71]
	v_mul_f32_e32 v68, v77, v68
	v_mul_f32_e32 v69, v77, v69
	v_fma_f32 v79, v68, v68, 0
	ds_write2_b32 v78, v68, v69 offset1:16
	s_waitcnt lgkmcnt(1)
	v_cvt_f32_f64_e32 v68, v[72:73]
	v_fmac_f32_e32 v79, v69, v69
	v_mul_f32_e32 v72, v77, v68
	ds_read2_b64 v[68:71], v76 offset0:64 offset1:80
	v_cvt_f32_f64_e32 v73, v[74:75]
	v_fmac_f32_e32 v79, v72, v72
	v_mul_f32_e32 v73, v77, v73
	v_fmac_f32_e32 v79, v73, v73
	ds_write2_b32 v78, v72, v73 offset0:32 offset1:48
	ds_read2_b64 v[72:75], v76 offset0:96 offset1:112
	s_waitcnt lgkmcnt(2)
	v_cvt_f32_f64_e32 v68, v[68:69]
	v_cvt_f32_f64_e32 v69, v[70:71]
	v_mul_f32_e32 v68, v77, v68
	v_mul_f32_e32 v69, v77, v69
	v_fmac_f32_e32 v79, v68, v68
	ds_write2_b32 v78, v68, v69 offset0:64 offset1:80
	s_waitcnt lgkmcnt(1)
	v_cvt_f32_f64_e32 v68, v[72:73]
	v_fmac_f32_e32 v79, v69, v69
	v_mul_f32_e32 v72, v77, v68
	ds_read2_b64 v[68:71], v76 offset0:128 offset1:144
	v_cvt_f32_f64_e32 v73, v[74:75]
	v_fmac_f32_e32 v79, v72, v72
	v_mul_f32_e32 v73, v77, v73
	v_fmac_f32_e32 v79, v73, v73
	ds_write2_b32 v78, v72, v73 offset0:96 offset1:112
	ds_read2_b64 v[72:75], v76 offset0:160 offset1:176
	s_waitcnt lgkmcnt(2)
	v_cvt_f32_f64_e32 v68, v[68:69]
	v_cvt_f32_f64_e32 v69, v[70:71]
	v_mul_f32_e32 v68, v77, v68
	v_mul_f32_e32 v69, v77, v69
	v_fmac_f32_e32 v79, v68, v68
	ds_write2_b32 v78, v68, v69 offset0:128 offset1:144
	s_waitcnt lgkmcnt(1)
	v_cvt_f32_f64_e32 v68, v[72:73]
	v_fmac_f32_e32 v79, v69, v69
	v_mul_f32_e32 v72, v77, v68
	ds_read2_b64 v[68:71], v76 offset0:192 offset1:208
	v_cvt_f32_f64_e32 v73, v[74:75]
	v_fmac_f32_e32 v79, v72, v72
	v_mul_f32_e32 v73, v77, v73
	v_fmac_f32_e32 v79, v73, v73
	ds_write2_b32 v78, v72, v73 offset0:160 offset1:176
	ds_read2_b64 v[72:75], v76 offset0:224 offset1:240
	s_waitcnt lgkmcnt(2)
	v_cvt_f32_f64_e32 v68, v[68:69]
	v_cvt_f32_f64_e32 v69, v[70:71]
	v_mul_f32_e32 v68, v77, v68
	v_mul_f32_e32 v69, v77, v69
	v_fmac_f32_e32 v79, v68, v68
	ds_write2_b32 v78, v68, v69 offset0:192 offset1:208
	s_waitcnt lgkmcnt(1)
	v_cvt_f32_f64_e32 v68, v[72:73]
	v_fmac_f32_e32 v79, v69, v69
	v_mul_f32_e32 v68, v77, v68
	v_cvt_f32_f64_e32 v69, v[74:75]
	v_fmac_f32_e32 v79, v68, v68
	v_mul_f32_e32 v69, v77, v69
	v_fmac_f32_e32 v79, v69, v69
	ds_write2_b32 v78, v68, v69 offset0:224 offset1:240
	v_cmp_eq_u32_e32 vcc, 0, v138
	v_add_f32_dpp v68, v79, v79 quad_perm:[1,0,3,2] row_mask:0xf bank_mask:0xf bound_ctrl:1
	s_nop 1
	v_add_f32_dpp v68, v68, v68 quad_perm:[2,3,0,1] row_mask:0xf bank_mask:0xf bound_ctrl:1
	s_nop 1
	v_add_f32_dpp v68, v68, v68 row_half_mirror row_mask:0xf bank_mask:0xf bound_ctrl:1
	s_nop 1
	v_mov_b32_dpp v69, v68 row_mirror row_mask:0xf bank_mask:0xf bound_ctrl:1
	s_and_saveexec_b64 s[0:1], vcc
	v_mov_b32_e32 v70, 0x11200
	v_lshl_or_b32 v67, v67, 2, v70
	v_add_f32_e32 v68, v68, v69
	ds_write_b32 v67, v68
	s_or_b64 exec, exec, s[0:1]
	v_lshlrev_b32_e32 v67, 2, v140
	s_movk_i32 s0, 0x408
	v_mad_u32_u24 v67, v138, s0, v67
	s_waitcnt lgkmcnt(0)
	s_barrier
	ds_read2_b32 v[68:69], v67 offset1:4
	ds_read2_b32 v[70:71], v67 offset0:64 offset1:68
	ds_read2_b32 v[72:73], v67 offset0:192 offset1:196
	s_lshl_b32 s29, s17, 2
	s_lshl_b32 s0, s24, 2
	s_waitcnt lgkmcnt(2)
	v_mfma_f32_16x16x4_f32 a[0:3], v68, v62, 0
	s_add_i32 s0, s0, 0x10100
	s_waitcnt lgkmcnt(1)
	v_mfma_f32_16x16x4_f32 a[4:7], v70, v63, 0
	ds_read2_b32 v[62:63], v67 offset0:128 offset1:132
	s_waitcnt lgkmcnt(0)
	v_mfma_f32_16x16x4_f32 a[0:3], v62, v64, a[0:3]
	v_mfma_f32_16x16x4_f32 a[4:7], v72, v65, a[4:7]
	v_mfma_f32_16x16x4_f32 a[0:3], v69, v58, a[0:3]
	v_mfma_f32_16x16x4_f32 a[4:7], v71, v59, a[4:7]
	ds_read2_b32 v[58:59], v67 offset0:8 offset1:12
	v_mfma_f32_16x16x4_f32 a[0:3], v63, v60, a[0:3]
	ds_read2_b32 v[62:63], v67 offset0:200 offset1:204
	v_mfma_f32_16x16x4_f32 a[4:7], v73, v61, a[4:7]
	ds_read2_b32 v[60:61], v67 offset0:72 offset1:76
	s_waitcnt lgkmcnt(2)
	v_mfma_f32_16x16x4_f32 a[0:3], v58, v54, a[0:3]
	s_waitcnt lgkmcnt(0)
	v_mfma_f32_16x16x4_f32 a[4:7], v60, v55, a[4:7]
	ds_read2_b32 v[54:55], v67 offset0:136 offset1:140
	s_waitcnt lgkmcnt(0)
	v_mfma_f32_16x16x4_f32 a[0:3], v54, v56, a[0:3]
	v_mfma_f32_16x16x4_f32 a[4:7], v62, v57, a[4:7]
	v_mfma_f32_16x16x4_f32 a[0:3], v59, v50, a[0:3]
	v_mfma_f32_16x16x4_f32 a[4:7], v61, v51, a[4:7]
	ds_read2_b32 v[50:51], v67 offset0:16 offset1:20
	v_mfma_f32_16x16x4_f32 a[0:3], v55, v52, a[0:3]
	ds_read2_b32 v[54:55], v67 offset0:208 offset1:212
	v_mfma_f32_16x16x4_f32 a[4:7], v63, v53, a[4:7]
	ds_read2_b32 v[52:53], v67 offset0:80 offset1:84
	s_waitcnt lgkmcnt(2)
	v_mfma_f32_16x16x4_f32 a[0:3], v50, v46, a[0:3]
	s_waitcnt lgkmcnt(0)
	v_mfma_f32_16x16x4_f32 a[4:7], v52, v47, a[4:7]
	ds_read2_b32 v[46:47], v67 offset0:144 offset1:148
	s_waitcnt lgkmcnt(0)
	v_mfma_f32_16x16x4_f32 a[0:3], v46, v48, a[0:3]
	v_mfma_f32_16x16x4_f32 a[4:7], v54, v49, a[4:7]
	v_mfma_f32_16x16x4_f32 a[0:3], v51, v42, a[0:3]
	v_mfma_f32_16x16x4_f32 a[4:7], v53, v43, a[4:7]
	ds_read2_b32 v[42:43], v67 offset0:24 offset1:28
	v_mfma_f32_16x16x4_f32 a[0:3], v47, v44, a[0:3]
	ds_read2_b32 v[46:47], v67 offset0:216 offset1:220
	v_mfma_f32_16x16x4_f32 a[4:7], v55, v45, a[4:7]
	ds_read2_b32 v[44:45], v67 offset0:88 offset1:92
	s_waitcnt lgkmcnt(2)
	v_mfma_f32_16x16x4_f32 a[0:3], v42, v38, a[0:3]
	s_waitcnt lgkmcnt(0)
	v_mfma_f32_16x16x4_f32 a[4:7], v44, v39, a[4:7]
	ds_read2_b32 v[38:39], v67 offset0:152 offset1:156
	s_waitcnt lgkmcnt(0)
	v_mfma_f32_16x16x4_f32 a[0:3], v38, v40, a[0:3]
	v_mfma_f32_16x16x4_f32 a[4:7], v46, v41, a[4:7]
	v_mfma_f32_16x16x4_f32 a[0:3], v43, v34, a[0:3]
	v_mfma_f32_16x16x4_f32 a[4:7], v45, v35, a[4:7]
	ds_read2_b32 v[34:35], v67 offset0:32 offset1:36
	v_mfma_f32_16x16x4_f32 a[0:3], v39, v36, a[0:3]
	ds_read2_b32 v[38:39], v67 offset0:224 offset1:228
	v_mfma_f32_16x16x4_f32 a[4:7], v47, v37, a[4:7]
	ds_read2_b32 v[36:37], v67 offset0:96 offset1:100
	s_waitcnt lgkmcnt(2)
	v_mfma_f32_16x16x4_f32 a[0:3], v34, v30, a[0:3]
	s_waitcnt lgkmcnt(0)
	v_mfma_f32_16x16x4_f32 a[4:7], v36, v31, a[4:7]
	ds_read2_b32 v[30:31], v67 offset0:160 offset1:164
	s_waitcnt lgkmcnt(0)
	v_mfma_f32_16x16x4_f32 a[0:3], v30, v32, a[0:3]
	v_mfma_f32_16x16x4_f32 a[4:7], v38, v33, a[4:7]
	v_mfma_f32_16x16x4_f32 a[0:3], v35, v26, a[0:3]
	v_mfma_f32_16x16x4_f32 a[4:7], v37, v27, a[4:7]
	ds_read2_b32 v[26:27], v67 offset0:40 offset1:44
	v_mfma_f32_16x16x4_f32 a[0:3], v31, v28, a[0:3]
	ds_read2_b32 v[30:31], v67 offset0:232 offset1:236
	v_mfma_f32_16x16x4_f32 a[4:7], v39, v29, a[4:7]
	ds_read2_b32 v[28:29], v67 offset0:104 offset1:108
	s_waitcnt lgkmcnt(2)
	v_mfma_f32_16x16x4_f32 a[0:3], v26, v22, a[0:3]
	s_waitcnt lgkmcnt(0)
	v_mfma_f32_16x16x4_f32 a[4:7], v28, v23, a[4:7]
	ds_read2_b32 v[22:23], v67 offset0:168 offset1:172
	s_waitcnt lgkmcnt(0)
	v_mfma_f32_16x16x4_f32 a[0:3], v22, v24, a[0:3]
	v_mfma_f32_16x16x4_f32 a[4:7], v30, v25, a[4:7]
	v_mfma_f32_16x16x4_f32 a[0:3], v27, v18, a[0:3]
	v_mfma_f32_16x16x4_f32 a[4:7], v29, v19, a[4:7]
	ds_read2_b32 v[18:19], v67 offset0:48 offset1:52
	v_mfma_f32_16x16x4_f32 a[0:3], v23, v20, a[0:3]
	ds_read2_b32 v[22:23], v67 offset0:240 offset1:244
	v_mfma_f32_16x16x4_f32 a[4:7], v31, v21, a[4:7]
	ds_read2_b32 v[20:21], v67 offset0:112 offset1:116
	s_waitcnt lgkmcnt(2)
	v_mfma_f32_16x16x4_f32 a[0:3], v18, v14, a[0:3]
	s_waitcnt lgkmcnt(0)
	v_mfma_f32_16x16x4_f32 a[4:7], v20, v15, a[4:7]
	ds_read2_b32 v[14:15], v67 offset0:176 offset1:180
	s_waitcnt lgkmcnt(0)
	v_mfma_f32_16x16x4_f32 a[0:3], v14, v16, a[0:3]
	v_mfma_f32_16x16x4_f32 a[4:7], v22, v17, a[4:7]
	v_mfma_f32_16x16x4_f32 a[0:3], v19, v10, a[0:3]
	v_mfma_f32_16x16x4_f32 a[4:7], v21, v11, a[4:7]
	ds_read2_b32 v[10:11], v67 offset0:56 offset1:60
	v_mfma_f32_16x16x4_f32 a[0:3], v15, v12, a[0:3]
	ds_read2_b32 v[14:15], v67 offset0:248 offset1:252
	v_mfma_f32_16x16x4_f32 a[4:7], v23, v13, a[4:7]
	ds_read2_b32 v[12:13], v67 offset0:120 offset1:124
	s_waitcnt lgkmcnt(2)
	v_mfma_f32_16x16x4_f32 a[0:3], v10, v6, a[0:3]
	s_waitcnt lgkmcnt(0)
	v_mfma_f32_16x16x4_f32 a[4:7], v12, v7, a[4:7]
	ds_read2_b32 v[6:7], v67 offset0:184 offset1:188
	s_waitcnt lgkmcnt(0)
	v_mfma_f32_16x16x4_f32 a[0:3], v6, v8, a[0:3]
	v_mfma_f32_16x16x4_f32 a[4:7], v14, v9, a[4:7]
	v_mfma_f32_16x16x4_f32 a[0:3], v11, v2, a[0:3]
	v_mov_b32_e32 v2, 0x11300
	v_lshl_add_u32 v2, v134, 2, v2
	ds_read_b32 v2, v2
	v_mfma_f32_16x16x4_f32 a[4:7], v13, v3, a[4:7]
	v_lshlrev_b32_e32 v3, 10, v140
	v_add3_u32 v3, s0, v66, v3
	v_mfma_f32_16x16x4_f32 a[0:3], v7, v4, a[0:3]
	v_or_b32_e32 v7, s29, v140
	v_lshl_or_b32 v4, v7, 8, v66
	v_add_u32_e32 v4, 0x10100, v4
	v_mfma_f32_16x16x4_f32 a[4:7], v15, v5, a[4:7]
	s_nop 9
	v_accvgpr_read_b32 v5, a0
	v_accvgpr_read_b32 v6, a1
	v_accvgpr_read_b32 v8, a2
	v_accvgpr_read_b32 v9, a3
	v_accvgpr_read_b32 v70, a4
	v_accvgpr_read_b32 v71, a5
	v_accvgpr_read_b32 v72, a6
	v_accvgpr_read_b32 v73, a7
	v_add_f32_e32 v5, v5, v70
	v_add_f32_e32 v6, v6, v71
	v_add_f32_e32 v8, v8, v72
	v_add_f32_e32 v9, v9, v73
	s_waitcnt lgkmcnt(0)
	v_fma_f32 v5, -2.0, v5, v2
	v_fma_f32 v6, -2.0, v6, v2
	v_fma_f32 v8, -2.0, v8, v2
	v_fmac_f32_e32 v2, -2.0, v9
	ds_write2st64_b32 v3, v5, v6 offset1:1
	ds_write2st64_b32 v3, v8, v2 offset0:2 offset1:3
	s_waitcnt lgkmcnt(0)
	s_barrier
	ds_read2_b32 v[2:3], v4 offset1:16
	ds_read2_b32 v[4:5], v4 offset0:32 offset1:48
	v_or_b32_e32 v6, 16, v138
	v_or_b32_e32 v8, 32, v138
	v_or_b32_e32 v9, 48, v138
	s_waitcnt lgkmcnt(1)
	v_cmp_lt_f32_e32 vcc, v3, v2
	s_nop 1
	v_cndmask_b32_e32 v10, v2, v3, vcc
	v_cndmask_b32_e32 v6, v138, v6, vcc
	s_waitcnt lgkmcnt(0)
	v_cmp_lt_f32_e32 vcc, v4, v10
	s_nop 1
	v_cndmask_b32_e32 v10, v10, v4, vcc
	v_cndmask_b32_e32 v8, v6, v8, vcc
	v_cmp_lt_f32_e32 vcc, v5, v10
	s_nop 1
	v_cndmask_b32_e32 v6, v10, v5, vcc
	v_cndmask_b32_e32 v14, v8, v9, vcc
	s_nop 0
	v_mov_b32_dpp v9, v6 quad_perm:[1,0,3,2] row_mask:0xf bank_mask:0xf bound_ctrl:1
	v_mov_b32_dpp v8, v14 quad_perm:[1,0,3,2] row_mask:0xf bank_mask:0xf bound_ctrl:1
	v_cmp_gt_f32_e64 s[4:5], v6, v9
	v_cmp_ngt_f32_e32 vcc, v6, v9
	s_and_saveexec_b64 s[6:7], vcc
	v_cmp_eq_f32_e32 vcc, v6, v9
	v_cmp_lt_i32_e64 s[0:1], v8, v14
	s_and_b64 s[0:1], vcc, s[0:1]
	s_andn2_b64 s[4:5], s[4:5], exec
	s_and_b64 s[0:1], s[0:1], exec
	s_or_b64 s[4:5], s[4:5], s[0:1]
	s_or_b64 exec, exec, s[6:7]
	s_and_saveexec_b64 s[0:1], s[4:5]
	v_mov_b32_e32 v6, v9
	v_mov_b32_e32 v14, v8
	s_or_b64 exec, exec, s[0:1]
	v_mov_b32_dpp v9, v6 quad_perm:[2,3,0,1] row_mask:0xf bank_mask:0xf bound_ctrl:1
	v_mov_b32_dpp v8, v14 quad_perm:[2,3,0,1] row_mask:0xf bank_mask:0xf bound_ctrl:1
	v_cmp_gt_f32_e64 s[4:5], v6, v9
	v_cmp_ngt_f32_e32 vcc, v6, v9
	s_and_saveexec_b64 s[6:7], vcc
	v_cmp_eq_f32_e32 vcc, v6, v9
	v_cmp_lt_i32_e64 s[0:1], v8, v14
	s_and_b64 s[0:1], vcc, s[0:1]
	s_andn2_b64 s[4:5], s[4:5], exec
	s_and_b64 s[0:1], s[0:1], exec
	s_or_b64 s[4:5], s[4:5], s[0:1]
	s_or_b64 exec, exec, s[6:7]
	s_and_saveexec_b64 s[0:1], s[4:5]
	v_mov_b32_e32 v6, v9
	v_mov_b32_e32 v14, v8
	s_or_b64 exec, exec, s[0:1]
	v_mov_b32_dpp v9, v6 row_half_mirror row_mask:0xf bank_mask:0xf bound_ctrl:1
	v_mov_b32_dpp v8, v14 row_half_mirror row_mask:0xf bank_mask:0xf bound_ctrl:1
	v_cmp_gt_f32_e64 s[4:5], v6, v9
	v_cmp_ngt_f32_e32 vcc, v6, v9
	s_and_saveexec_b64 s[6:7], vcc
	v_cmp_eq_f32_e32 vcc, v6, v9
	v_cmp_lt_i32_e64 s[0:1], v8, v14
	s_and_b64 s[0:1], vcc, s[0:1]
	s_andn2_b64 s[4:5], s[4:5], exec
	s_and_b64 s[0:1], s[0:1], exec
	s_or_b64 s[4:5], s[4:5], s[0:1]
	s_or_b64 exec, exec, s[6:7]
	s_and_saveexec_b64 s[0:1], s[4:5]
	v_mov_b32_e32 v6, v9
	v_mov_b32_e32 v14, v8
	s_or_b64 exec, exec, s[0:1]
	v_mov_b32_dpp v8, v6 row_mirror row_mask:0xf bank_mask:0xf bound_ctrl:1
	v_mov_b32_dpp v9, v14 row_mirror row_mask:0xf bank_mask:0xf bound_ctrl:1
	v_cmp_gt_f32_e64 s[4:5], v6, v8
	v_cmp_ngt_f32_e32 vcc, v6, v8
	s_and_saveexec_b64 s[6:7], vcc
	v_cmp_eq_f32_e32 vcc, v6, v8
	v_cmp_lt_i32_e64 s[0:1], v9, v14
	s_and_b64 s[0:1], vcc, s[0:1]
	s_andn2_b64 s[4:5], s[4:5], exec
	s_and_b64 s[0:1], s[0:1], exec
	s_or_b64 s[4:5], s[4:5], s[0:1]
	s_or_b64 exec, exec, s[6:7]
	s_and_saveexec_b64 s[0:1], s[4:5]
	v_mov_b32_e32 v6, v8
	v_mov_b32_e32 v14, v9
	s_or_b64 exec, exec, s[0:1]
	v_mov_b32_e32 v8, 0x11300
	v_lshl_or_b32 v8, v1, 2, v8
	ds_read_b32 v8, v8
	v_mov_b32_e32 v9, 0x11200
	v_lshl_add_u32 v7, v7, 2, v9
	ds_read_b32 v9, v7
	v_mov_b32_e32 v13, 0x260
	s_waitcnt lgkmcnt(1)
	v_mov_b32_dpp v7, v8 quad_perm:[1,0,3,2] row_mask:0xf bank_mask:0xf bound_ctrl:1
	v_max_f32_e32 v8, v8, v8
	v_max_f32_e32 v7, v7, v7
	v_max_f32_e32 v7, v8, v7
	v_lshlrev_b32_e32 v18, 2, v139
	v_mov_b32_e32 v19, 0
	v_mov_b32_dpp v8, v7 quad_perm:[2,3,0,1] row_mask:0xf bank_mask:0xf bound_ctrl:1
	v_max_f32_e32 v8, v8, v8
	v_max_f32_e32 v7, v7, v8
	s_mov_b32 s25, 0
	s_mov_b32 s26, s25
	v_mov_b32_dpp v8, v7 row_half_mirror row_mask:0xf bank_mask:0xf bound_ctrl:1
	v_max_f32_e32 v8, v8, v8
	v_max_f32_e32 v7, v7, v8
	s_nop 1
	v_mov_b32_dpp v8, v7 row_mirror row_mask:0xf bank_mask:0xf bound_ctrl:1
	v_max_f32_e32 v8, v8, v8
	v_max_f32_e32 v7, v7, v8
	s_nop 0
	v_readlane_b32 s4, v7, 32
	v_readlane_b32 s5, v7, 48
	v_readlane_b32 s0, v7, 0
	v_readlane_b32 s1, v7, 16
	v_max_f32_e64 v7, s5, s5
	v_max_f32_e64 v8, s4, s4
	v_max_f32_e32 v7, v8, v7
	v_mov_b32_e32 v8, s1
	v_max3_f32 v8, s0, v8, v7
	s_mov_b32 s0, 0x3f800347
	s_mov_b32 s1, 0x3f8020c5
	s_waitcnt lgkmcnt(0)
	v_pk_mul_f32 v[8:9], v[8:9], s[0:1]
	s_mov_b32 s4, 0xf800000
	v_mul_f32_e32 v7, 0x4f800000, v9
	v_cmp_gt_f32_e32 vcc, s4, v9
	s_nop 1
	v_cndmask_b32_e32 v7, v9, v7, vcc
	v_sqrt_f32_e32 v10, v7
	s_nop 0
	v_add_u32_e32 v11, -1, v10
	v_fma_f32 v12, -v11, v10, v7
	v_cmp_ge_f32_e64 s[0:1], 0, v12
	v_add_u32_e32 v12, 1, v10
	s_nop 0
	v_cndmask_b32_e64 v11, v10, v11, s[0:1]
	v_fma_f32 v10, -v12, v10, v7
	v_cmp_lt_f32_e64 s[0:1], 0, v10
	s_nop 1
	v_cndmask_b32_e64 v10, v11, v12, s[0:1]
	v_mul_f32_e32 v11, 0x37800000, v10
	v_cndmask_b32_e32 v10, v10, v11, vcc
	v_mul_f32_e32 v11, 0x4f800000, v8
	v_cmp_gt_f32_e32 vcc, s4, v8
	v_cmp_class_f32_e64 s[0:1], v7, v13
	s_nop 0
	v_cndmask_b32_e32 v11, v8, v11, vcc
	v_sqrt_f32_e32 v12, v11
	v_cndmask_b32_e64 v7, v10, v7, s[0:1]
	v_add_u32_e32 v10, -1, v12
	v_fma_f32 v15, -v10, v12, v11
	v_cmp_ge_f32_e64 s[0:1], 0, v15
	v_add_u32_e32 v15, 1, v12
	s_nop 0
	v_cndmask_b32_e64 v10, v12, v10, s[0:1]
	v_fma_f32 v12, -v15, v12, v11
	v_cmp_lt_f32_e64 s[0:1], 0, v12
	s_nop 1
	v_cndmask_b32_e64 v10, v10, v15, s[0:1]
	v_mul_f32_e32 v12, 0x37800000, v10
	v_cndmask_b32_e32 v10, v10, v12, vcc
	v_cmp_class_f32_e32 vcc, v11, v13
	s_mov_b32 s0, 0x380637bd
	s_mov_b32 s1, 0x350637bd
	v_cndmask_b32_e32 v10, v10, v11, vcc
	v_mul_f32_e32 v7, v7, v10
	v_mul_f32_e32 v7, 0x3f800347, v7
	v_pk_mul_f32 v[8:9], v[8:9], s[0:1]
	s_nop 0
	v_fmamk_f32 v7, v7, 0x3888509c, v9
	v_add_f32_e32 v7, v8, v7
	v_add_f32_e32 v7, 0xda24260, v7
	v_add_f32_e32 v6, v6, v7
	v_cmp_le_f32_e64 s[8:9], v2, v6
	v_cmp_le_f32_e64 s[6:7], v3, v6
	v_cmp_le_f32_e64 s[4:5], v4, v6
	v_lshl_add_u64 v[2:3], s[22:23], 0, v[18:19]
	s_and_b32 s19, s8, 0xffff
	s_lshl_b32 s22, s6, 16
	v_cmp_le_f32_e64 s[0:1], v5, v6
	s_or_b32 s24, s19, s22
	s_and_b32 s23, s4, 0xffff
	s_mov_b32 s22, s25
	s_or_b64 s[22:23], s[24:25], s[22:23]
	s_lshl_b32 s27, s0, 16
	s_or_b64 s[26:27], s[22:23], s[26:27]
	s_add_u32 s22, s26, -1
	s_addc_u32 s23, s27, -1
	s_and_b64 s[22:23], s[26:27], s[22:23]
	s_cmp_eq_u64 s[22:23], 0
	v_readlane_b32 s22, v14, 0
	s_cbranch_scc1 .LBB0_139
	s_bcnt1_i32_b64 s60, s[26:27]
	s_cmp_lg_u32 s60, 2
	s_cbranch_scc1 .Lslowc_0
	s_ff1_i32_b64 s61, s[26:27]
	s_mov_b64 s[62:63], s[26:27]
	s_bitset0_b64 s[62:63], s61
	s_ff1_i32_b64 s64, s[62:63]
	s_lshl_b32 s66, s61, 10
	s_mov_b32 s67, 0
	v_lshl_add_u64 v[66:67], v[2:3], 0, s[66:67]
	global_load_dwordx4 v[70:73], v[66:67], off
	s_lshl_b32 s66, s64, 10
	v_lshl_add_u64 v[68:69], v[2:3], 0, s[66:67]
	global_load_dwordx4 v[74:77], v[68:69], off
	s_add_i32 s65, s29, 0
	s_lshl_b32 s66, s65, 2
	s_add_i32 s66, s66, 0x11100
	v_mov_b32_e32 v78, s66
	ds_read_b32 v78, v78
	s_mul_i32 s66, s65, 0x810
	v_add_u32_e32 v79, s66, v135
	ds_read2st64_b64 v[80:83], v79 offset0:64 offset1:65
	ds_read2st64_b64 v[84:87], v79 offset0:66 offset1:67
	s_waitcnt lgkmcnt(2)
	v_max_i32_e32 v78, 1, v78
	v_cvt_f64_u32_e32 v[88:89], v78
	v_div_scale_f64 v[90:91], s[68:69], v[88:89], v[88:89], 1.0
	v_rcp_f64_e32 v[92:93], v[90:91]
	v_div_scale_f64 v[94:95], vcc, 1.0, v[88:89], 1.0
	v_fma_f64 v[96:97], -v[90:91], v[92:93], 1.0
	v_fmac_f64_e32 v[92:93], v[92:93], v[96:97]
	v_fma_f64 v[96:97], -v[90:91], v[92:93], 1.0
	v_fmac_f64_e32 v[92:93], v[92:93], v[96:97]
	v_mul_f64 v[96:97], v[94:95], v[92:93]
	v_fma_f64 v[90:91], -v[90:91], v[96:97], v[94:95]
	v_div_fmas_f64 v[90:91], v[90:91], v[92:93], v[96:97]
	v_div_fixup_f64 v[88:89], v[90:91], v[88:89], 1.0
	s_waitcnt lgkmcnt(0)
	v_mul_f64 v[82:83], v[82:83], v[88:89]
	v_mul_f64 v[80:81], v[80:81], v[88:89]
	v_mul_f64 v[84:85], v[84:85], v[88:89]
	v_mul_f64 v[86:87], v[88:89], v[86:87]
	v_mul_f64 v[100:101], v[82:83], v[82:83]
	v_fmac_f64_e32 v[100:101], v[80:81], v[80:81]
	v_fmac_f64_e32 v[100:101], v[84:85], v[84:85]
	v_fmac_f64_e32 v[100:101], v[86:87], v[86:87]
	s_waitcnt vmcnt(0)
	v_cvt_f64_f32_e32 v[110:111], v70
	v_cvt_f64_f32_e32 v[112:113], v71
	v_cvt_f64_f32_e32 v[114:115], v72
	v_cvt_f64_f32_e32 v[116:117], v73
	v_mul_f64 v[102:103], v[82:83], v[112:113]
	v_mul_f64 v[104:105], v[112:113], v[112:113]
	v_fmac_f64_e32 v[102:103], v[80:81], v[110:111]
	v_fmac_f64_e32 v[104:105], v[110:111], v[110:111]
	v_fmac_f64_e32 v[102:103], v[84:85], v[114:115]
	v_fmac_f64_e32 v[104:105], v[114:115], v[114:115]
	v_fmac_f64_e32 v[102:103], v[86:87], v[116:117]
	v_fmac_f64_e32 v[104:105], v[116:117], v[116:117]
	v_cvt_f64_f32_e32 v[110:111], v74
	v_cvt_f64_f32_e32 v[112:113], v75
	v_cvt_f64_f32_e32 v[114:115], v76
	v_cvt_f64_f32_e32 v[116:117], v77
	v_mul_f64 v[106:107], v[82:83], v[112:113]
	v_mul_f64 v[108:109], v[112:113], v[112:113]
	v_fmac_f64_e32 v[106:107], v[80:81], v[110:111]
	v_fmac_f64_e32 v[108:109], v[110:111], v[110:111]
	v_fmac_f64_e32 v[106:107], v[84:85], v[114:115]
	v_fmac_f64_e32 v[108:109], v[114:115], v[114:115]
	v_fmac_f64_e32 v[106:107], v[86:87], v[116:117]
	v_fmac_f64_e32 v[108:109], v[116:117], v[116:117]
	s_nop 1
	v_mov_b32_dpp v120, v100 quad_perm:[1,0,3,2] row_mask:0xf bank_mask:0xf bound_ctrl:1
	v_mov_b32_dpp v121, v101 quad_perm:[1,0,3,2] row_mask:0xf bank_mask:0xf bound_ctrl:1
	v_mov_b32_dpp v122, v102 quad_perm:[1,0,3,2] row_mask:0xf bank_mask:0xf bound_ctrl:1
	v_mov_b32_dpp v123, v103 quad_perm:[1,0,3,2] row_mask:0xf bank_mask:0xf bound_ctrl:1
	v_mov_b32_dpp v124, v104 quad_perm:[1,0,3,2] row_mask:0xf bank_mask:0xf bound_ctrl:1
	v_mov_b32_dpp v125, v105 quad_perm:[1,0,3,2] row_mask:0xf bank_mask:0xf bound_ctrl:1
	v_mov_b32_dpp v126, v106 quad_perm:[1,0,3,2] row_mask:0xf bank_mask:0xf bound_ctrl:1
	v_mov_b32_dpp v127, v107 quad_perm:[1,0,3,2] row_mask:0xf bank_mask:0xf bound_ctrl:1
	v_mov_b32_dpp v128, v108 quad_perm:[1,0,3,2] row_mask:0xf bank_mask:0xf bound_ctrl:1
	v_mov_b32_dpp v129, v109 quad_perm:[1,0,3,2] row_mask:0xf bank_mask:0xf bound_ctrl:1
	v_add_f64 v[100:101], v[100:101], v[120:121]
	v_add_f64 v[102:103], v[102:103], v[122:123]
	v_add_f64 v[104:105], v[104:105], v[124:125]
	v_add_f64 v[106:107], v[106:107], v[126:127]
	v_add_f64 v[108:109], v[108:109], v[128:129]
	s_nop 1
	v_mov_b32_dpp v120, v100 quad_perm:[2,3,0,1] row_mask:0xf bank_mask:0xf bound_ctrl:1
	v_mov_b32_dpp v121, v101 quad_perm:[2,3,0,1] row_mask:0xf bank_mask:0xf bound_ctrl:1
	v_mov_b32_dpp v122, v102 quad_perm:[2,3,0,1] row_mask:0xf bank_mask:0xf bound_ctrl:1
	v_mov_b32_dpp v123, v103 quad_perm:[2,3,0,1] row_mask:0xf bank_mask:0xf bound_ctrl:1
	v_mov_b32_dpp v124, v104 quad_perm:[2,3,0,1] row_mask:0xf bank_mask:0xf bound_ctrl:1
	v_mov_b32_dpp v125, v105 quad_perm:[2,3,0,1] row_mask:0xf bank_mask:0xf bound_ctrl:1
	v_mov_b32_dpp v126, v106 quad_perm:[2,3,0,1] row_mask:0xf bank_mask:0xf bound_ctrl:1
	v_mov_b32_dpp v127, v107 quad_perm:[2,3,0,1] row_mask:0xf bank_mask:0xf bound_ctrl:1
	v_mov_b32_dpp v128, v108 quad_perm:[2,3,0,1] row_mask:0xf bank_mask:0xf bound_ctrl:1
	v_mov_b32_dpp v129, v109 quad_perm:[2,3,0,1] row_mask:0xf bank_mask:0xf bound_ctrl:1
	v_add_f64 v[100:101], v[100:101], v[120:121]
	v_add_f64 v[102:103], v[102:103], v[122:123]
	v_add_f64 v[104:105], v[104:105], v[124:125]
	v_add_f64 v[106:107], v[106:107], v[126:127]
	v_add_f64 v[108:109], v[108:109], v[128:129]
	s_nop 1
	v_mov_b32_dpp v120, v100 row_half_mirror row_mask:0xf bank_mask:0xf bound_ctrl:1
	v_mov_b32_dpp v121, v101 row_half_mirror row_mask:0xf bank_mask:0xf bound_ctrl:1
	v_mov_b32_dpp v122, v102 row_half_mirror row_mask:0xf bank_mask:0xf bound_ctrl:1
	v_mov_b32_dpp v123, v103 row_half_mirror row_mask:0xf bank_mask:0xf bound_ctrl:1
	v_mov_b32_dpp v124, v104 row_half_mirror row_mask:0xf bank_mask:0xf bound_ctrl:1
	v_mov_b32_dpp v125, v105 row_half_mirror row_mask:0xf bank_mask:0xf bound_ctrl:1
	v_mov_b32_dpp v126, v106 row_half_mirror row_mask:0xf bank_mask:0xf bound_ctrl:1
	v_mov_b32_dpp v127, v107 row_half_mirror row_mask:0xf bank_mask:0xf bound_ctrl:1
	v_mov_b32_dpp v128, v108 row_half_mirror row_mask:0xf bank_mask:0xf bound_ctrl:1
	v_mov_b32_dpp v129, v109 row_half_mirror row_mask:0xf bank_mask:0xf bound_ctrl:1
	v_add_f64 v[100:101], v[100:101], v[120:121]
	v_add_f64 v[102:103], v[102:103], v[122:123]
	v_add_f64 v[104:105], v[104:105], v[124:125]
	v_add_f64 v[106:107], v[106:107], v[126:127]
	v_add_f64 v[108:109], v[108:109], v[128:129]
	s_nop 1
	v_mov_b32_dpp v120, v100 row_mirror row_mask:0xf bank_mask:0xf bound_ctrl:1
	v_mov_b32_dpp v121, v101 row_mirror row_mask:0xf bank_mask:0xf bound_ctrl:1
	v_mov_b32_dpp v122, v102 row_mirror row_mask:0xf bank_mask:0xf bound_ctrl:1
	v_mov_b32_dpp v123, v103 row_mirror row_mask:0xf bank_mask:0xf bound_ctrl:1
	v_mov_b32_dpp v124, v104 row_mirror row_mask:0xf bank_mask:0xf bound_ctrl:1
	v_mov_b32_dpp v125, v105 row_mirror row_mask:0xf bank_mask:0xf bound_ctrl:1
	v_mov_b32_dpp v126, v106 row_mirror row_mask:0xf bank_mask:0xf bound_ctrl:1
	v_mov_b32_dpp v127, v107 row_mirror row_mask:0xf bank_mask:0xf bound_ctrl:1
	v_mov_b32_dpp v128, v108 row_mirror row_mask:0xf bank_mask:0xf bound_ctrl:1
	v_mov_b32_dpp v129, v109 row_mirror row_mask:0xf bank_mask:0xf bound_ctrl:1
	v_add_f64 v[100:101], v[100:101], v[120:121]
	v_add_f64 v[102:103], v[102:103], v[122:123]
	v_add_f64 v[104:105], v[104:105], v[124:125]
	v_add_f64 v[106:107], v[106:107], v[126:127]
	v_add_f64 v[108:109], v[108:109], v[128:129]
	s_nop 0
	v_readlane_b32 s70, v100, 0
	v_readlane_b32 s71, v101, 0
	v_readlane_b32 s72, v100, 16
	v_readlane_b32 s73, v101, 16
	v_readlane_b32 s74, v100, 32
	v_readlane_b32 s75, v101, 32
	v_readlane_b32 s76, v100, 48
	v_readlane_b32 s77, v101, 48
	v_mov_b32_e32 v130, s72
	v_mov_b32_e32 v131, s73
	v_mov_b32_e32 v132, s76
	v_mov_b32_e32 v133, s77
	v_add_f64 v[130:131], s[70:71], v[130:131]
	v_add_f64 v[132:133], s[74:75], v[132:133]
	v_add_f64 v[100:101], v[130:131], v[132:133]
	v_readlane_b32 s70, v102, 0
	v_readlane_b32 s71, v103, 0
	v_readlane_b32 s72, v102, 16
	v_readlane_b32 s73, v103, 16
	v_readlane_b32 s74, v102, 32
	v_readlane_b32 s75, v103, 32
	v_readlane_b32 s76, v102, 48
	v_readlane_b32 s77, v103, 48
	v_mov_b32_e32 v130, s72
	v_mov_b32_e32 v131, s73
	v_mov_b32_e32 v132, s76
	v_mov_b32_e32 v133, s77
	v_add_f64 v[130:131], s[70:71], v[130:131]
	v_add_f64 v[132:133], s[74:75], v[132:133]
	v_add_f64 v[102:103], v[130:131], v[132:133]
	v_readlane_b32 s70, v104, 0
	v_readlane_b32 s71, v105, 0
	v_readlane_b32 s72, v104, 16
	v_readlane_b32 s73, v105, 16
	v_readlane_b32 s74, v104, 32
	v_readlane_b32 s75, v105, 32
	v_readlane_b32 s76, v104, 48
	v_readlane_b32 s77, v105, 48
	v_mov_b32_e32 v130, s72
	v_mov_b32_e32 v131, s73
	v_mov_b32_e32 v132, s76
	v_mov_b32_e32 v133, s77
	v_add_f64 v[130:131], s[70:71], v[130:131]
	v_add_f64 v[132:133], s[74:75], v[132:133]
	v_add_f64 v[104:105], v[130:131], v[132:133]
	v_readlane_b32 s70, v106, 0
	v_readlane_b32 s71, v107, 0
	v_readlane_b32 s72, v106, 16
	v_readlane_b32 s73, v107, 16
	v_readlane_b32 s74, v106, 32
	v_readlane_b32 s75, v107, 32
	v_readlane_b32 s76, v106, 48
	v_readlane_b32 s77, v107, 48
	v_mov_b32_e32 v130, s72
	v_mov_b32_e32 v131, s73
	v_mov_b32_e32 v132, s76
	v_mov_b32_e32 v133, s77
	v_add_f64 v[130:131], s[70:71], v[130:131]
	v_add_f64 v[132:133], s[74:75], v[132:133]
	v_add_f64 v[106:107], v[130:131], v[132:133]
	v_readlane_b32 s70, v108, 0
	v_readlane_b32 s71, v109, 0
	v_readlane_b32 s72, v108, 16
	v_readlane_b32 s73, v109, 16
	v_readlane_b32 s74, v108, 32
	v_readlane_b32 s75, v109, 32
	v_readlane_b32 s76, v108, 48
	v_readlane_b32 s77, v109, 48
	v_mov_b32_e32 v130, s72
	v_mov_b32_e32 v131, s73
	v_mov_b32_e32 v132, s76
	v_mov_b32_e32 v133, s77
	v_add_f64 v[130:131], s[70:71], v[130:131]
	v_add_f64 v[132:133], s[74:75], v[132:133]
	v_add_f64 v[108:109], v[130:131], v[132:133]
	v_add_f64 v[104:105], v[100:101], v[104:105]
	v_fmac_f64_e32 v[104:105], -2.0, v[102:103]
	v_add_f64 v[108:109], v[100:101], v[108:109]
	v_fmac_f64_e32 v[108:109], -2.0, v[106:107]
	v_cvt_f32_f64_e32 v110, v[104:105]
	v_cvt_f32_f64_e32 v111, v[108:109]
	v_cmp_gt_f32_e32 vcc, v110, v111
	s_nop 1
	s_and_b64 s[68:69], vcc, exec
	s_cselect_b32 s22, s64, s61
	s_branch .LBB0_139
.Lslowc_0:
	s_lshl_b32 s19, s29, 2
	s_add_i32 s19, s19, 0x11100
	v_mov_b32_e32 v4, s19
	ds_read_b32 v4, v4
	s_mul_i32 s19, s17, 0x2040
	v_add_u32_e32 v8, s19, v135
	v_mov_b32_e32 v15, 0x7f800000
	s_waitcnt lgkmcnt(0)
	v_max_i32_e32 v4, 1, v4
	v_cvt_f64_u32_e32 v[12:13], v4
	v_div_scale_f64 v[16:17], s[30:31], v[12:13], v[12:13], 1.0
	v_rcp_f64_e32 v[20:21], v[16:17]
	v_div_scale_f64 v[22:23], vcc, 1.0, v[12:13], 1.0
	ds_read2st64_b64 v[4:7], v8 offset0:64 offset1:65
	ds_read2st64_b64 v[8:11], v8 offset0:66 offset1:67
	v_fma_f64 v[24:25], -v[16:17], v[20:21], 1.0
	v_fmac_f64_e32 v[20:21], v[20:21], v[24:25]
	v_fma_f64 v[24:25], -v[16:17], v[20:21], 1.0
	v_fmac_f64_e32 v[20:21], v[20:21], v[24:25]
	v_mul_f64 v[24:25], v[22:23], v[20:21]
	v_fma_f64 v[16:17], -v[16:17], v[24:25], v[22:23]
	v_div_fmas_f64 v[16:17], v[16:17], v[20:21], v[24:25]
	v_div_fixup_f64 v[12:13], v[16:17], v[12:13], 1.0
	s_waitcnt lgkmcnt(1)
	v_mul_f64 v[6:7], v[6:7], v[12:13]
	v_mul_f64 v[4:5], v[4:5], v[12:13]
	s_waitcnt lgkmcnt(0)
	v_mul_f64 v[8:9], v[8:9], v[12:13]
	v_mul_f64 v[10:11], v[12:13], v[10:11]
	v_mul_f64 v[12:13], v[6:7], v[6:7]
	v_fmac_f64_e32 v[12:13], v[4:5], v[4:5]
	v_fmac_f64_e32 v[12:13], v[8:9], v[8:9]
	v_fmac_f64_e32 v[12:13], v[10:11], v[10:11]
	s_nop 1
	v_mov_b32_dpp v16, v12 quad_perm:[1,0,3,2] row_mask:0xf bank_mask:0xf bound_ctrl:1
	v_mov_b32_dpp v17, v13 quad_perm:[1,0,3,2] row_mask:0xf bank_mask:0xf bound_ctrl:1
	v_add_f64 v[12:13], v[12:13], v[16:17]
	s_nop 1
	v_mov_b32_dpp v16, v12 quad_perm:[2,3,0,1] row_mask:0xf bank_mask:0xf bound_ctrl:1
	v_mov_b32_dpp v17, v13 quad_perm:[2,3,0,1] row_mask:0xf bank_mask:0xf bound_ctrl:1
	v_add_f64 v[12:13], v[12:13], v[16:17]
	s_nop 1
	v_mov_b32_dpp v16, v12 row_half_mirror row_mask:0xf bank_mask:0xf bound_ctrl:1
	v_mov_b32_dpp v17, v13 row_half_mirror row_mask:0xf bank_mask:0xf bound_ctrl:1
	v_add_f64 v[12:13], v[12:13], v[16:17]
	s_nop 1
	v_mov_b32_dpp v16, v12 row_mirror row_mask:0xf bank_mask:0xf bound_ctrl:1
	v_mov_b32_dpp v17, v13 row_mirror row_mask:0xf bank_mask:0xf bound_ctrl:1
	v_add_f64 v[12:13], v[12:13], v[16:17]
	s_nop 0
	v_readlane_b32 s19, v13, 16
	v_readlane_b32 s23, v12, 16
	v_readlane_b32 s31, v13, 0
	v_readlane_b32 s30, v12, 0
	v_mov_b32_e32 v16, s23
	v_mov_b32_e32 v17, s19
	v_readlane_b32 s19, v13, 48
	v_readlane_b32 s23, v12, 48
	v_add_f64 v[16:17], s[30:31], v[16:17]
	v_readlane_b32 s31, v13, 32
	v_readlane_b32 s30, v12, 32
	v_mov_b32_e32 v12, s23
	v_mov_b32_e32 v13, s19
	v_add_f64 v[12:13], s[30:31], v[12:13]
	v_add_f64 v[12:13], v[16:17], v[12:13]

.LBB0_139:
	s_lshr_b32 s8, s8, 16
	s_and_b32 s19, s6, 0xffff0000
	s_mov_b32 s25, 0
	s_lshl_b64 s[26:27], s[4:5], 16
	s_or_b32 s24, s19, s8
	s_and_b32 s27, s27, 0xffff
	s_mov_b32 s26, s25
	s_or_b64 s[26:27], s[24:25], s[26:27]
	s_and_b32 s31, s0, 0xffff0000
	s_mov_b32 s30, s25
	s_or_b64 s[26:27], s[26:27], s[30:31]
	s_add_u32 s30, s26, -1
	s_addc_u32 s31, s27, -1
	s_and_b64 s[30:31], s[26:27], s[30:31]
	s_cmp_eq_u64 s[30:31], 0
	v_readlane_b32 s8, v14, 16
	s_cbranch_scc1 .LBB0_142
	s_bcnt1_i32_b64 s60, s[26:27]
	s_cmp_lg_u32 s60, 2
	s_cbranch_scc1 .Lslowc_1
	s_ff1_i32_b64 s61, s[26:27]
	s_mov_b64 s[62:63], s[26:27]
	s_bitset0_b64 s[62:63], s61
	s_ff1_i32_b64 s64, s[62:63]
	s_lshl_b32 s66, s61, 10
	s_mov_b32 s67, 0
	v_lshl_add_u64 v[66:67], v[2:3], 0, s[66:67]
	global_load_dwordx4 v[70:73], v[66:67], off
	s_lshl_b32 s66, s64, 10
	v_lshl_add_u64 v[68:69], v[2:3], 0, s[66:67]
	global_load_dwordx4 v[74:77], v[68:69], off
	s_add_i32 s65, s29, 1
	s_lshl_b32 s66, s65, 2
	s_add_i32 s66, s66, 0x11100
	v_mov_b32_e32 v78, s66
	ds_read_b32 v78, v78
	s_mul_i32 s66, s65, 0x810
	v_add_u32_e32 v79, s66, v135
	ds_read2st64_b64 v[80:83], v79 offset0:64 offset1:65
	ds_read2st64_b64 v[84:87], v79 offset0:66 offset1:67
	s_waitcnt lgkmcnt(2)
	v_max_i32_e32 v78, 1, v78
	v_cvt_f64_u32_e32 v[88:89], v78
	v_div_scale_f64 v[90:91], s[68:69], v[88:89], v[88:89], 1.0
	v_rcp_f64_e32 v[92:93], v[90:91]
	v_div_scale_f64 v[94:95], vcc, 1.0, v[88:89], 1.0
	v_fma_f64 v[96:97], -v[90:91], v[92:93], 1.0
	v_fmac_f64_e32 v[92:93], v[92:93], v[96:97]
	v_fma_f64 v[96:97], -v[90:91], v[92:93], 1.0
	v_fmac_f64_e32 v[92:93], v[92:93], v[96:97]
	v_mul_f64 v[96:97], v[94:95], v[92:93]
	v_fma_f64 v[90:91], -v[90:91], v[96:97], v[94:95]
	v_div_fmas_f64 v[90:91], v[90:91], v[92:93], v[96:97]
	v_div_fixup_f64 v[88:89], v[90:91], v[88:89], 1.0
	s_waitcnt lgkmcnt(0)
	v_mul_f64 v[82:83], v[82:83], v[88:89]
	v_mul_f64 v[80:81], v[80:81], v[88:89]
	v_mul_f64 v[84:85], v[84:85], v[88:89]
	v_mul_f64 v[86:87], v[88:89], v[86:87]
	v_mul_f64 v[100:101], v[82:83], v[82:83]
	v_fmac_f64_e32 v[100:101], v[80:81], v[80:81]
	v_fmac_f64_e32 v[100:101], v[84:85], v[84:85]
	v_fmac_f64_e32 v[100:101], v[86:87], v[86:87]
	s_waitcnt vmcnt(0)
	v_cvt_f64_f32_e32 v[110:111], v70
	v_cvt_f64_f32_e32 v[112:113], v71
	v_cvt_f64_f32_e32 v[114:115], v72
	v_cvt_f64_f32_e32 v[116:117], v73
	v_mul_f64 v[102:103], v[82:83], v[112:113]
	v_mul_f64 v[104:105], v[112:113], v[112:113]
	v_fmac_f64_e32 v[102:103], v[80:81], v[110:111]
	v_fmac_f64_e32 v[104:105], v[110:111], v[110:111]
	v_fmac_f64_e32 v[102:103], v[84:85], v[114:115]
	v_fmac_f64_e32 v[104:105], v[114:115], v[114:115]
	v_fmac_f64_e32 v[102:103], v[86:87], v[116:117]
	v_fmac_f64_e32 v[104:105], v[116:117], v[116:117]
	v_cvt_f64_f32_e32 v[110:111], v74
	v_cvt_f64_f32_e32 v[112:113], v75
	v_cvt_f64_f32_e32 v[114:115], v76
	v_cvt_f64_f32_e32 v[116:117], v77
	v_mul_f64 v[106:107], v[82:83], v[112:113]
	v_mul_f64 v[108:109], v[112:113], v[112:113]
	v_fmac_f64_e32 v[106:107], v[80:81], v[110:111]
	v_fmac_f64_e32 v[108:109], v[110:111], v[110:111]
	v_fmac_f64_e32 v[106:107], v[84:85], v[114:115]
	v_fmac_f64_e32 v[108:109], v[114:115], v[114:115]
	v_fmac_f64_e32 v[106:107], v[86:87], v[116:117]
	v_fmac_f64_e32 v[108:109], v[116:117], v[116:117]
	s_nop 1
	v_mov_b32_dpp v120, v100 quad_perm:[1,0,3,2] row_mask:0xf bank_mask:0xf bound_ctrl:1
	v_mov_b32_dpp v121, v101 quad_perm:[1,0,3,2] row_mask:0xf bank_mask:0xf bound_ctrl:1
	v_mov_b32_dpp v122, v102 quad_perm:[1,0,3,2] row_mask:0xf bank_mask:0xf bound_ctrl:1
	v_mov_b32_dpp v123, v103 quad_perm:[1,0,3,2] row_mask:0xf bank_mask:0xf bound_ctrl:1
	v_mov_b32_dpp v124, v104 quad_perm:[1,0,3,2] row_mask:0xf bank_mask:0xf bound_ctrl:1
	v_mov_b32_dpp v125, v105 quad_perm:[1,0,3,2] row_mask:0xf bank_mask:0xf bound_ctrl:1
	v_mov_b32_dpp v126, v106 quad_perm:[1,0,3,2] row_mask:0xf bank_mask:0xf bound_ctrl:1
	v_mov_b32_dpp v127, v107 quad_perm:[1,0,3,2] row_mask:0xf bank_mask:0xf bound_ctrl:1
	v_mov_b32_dpp v128, v108 quad_perm:[1,0,3,2] row_mask:0xf bank_mask:0xf bound_ctrl:1
	v_mov_b32_dpp v129, v109 quad_perm:[1,0,3,2] row_mask:0xf bank_mask:0xf bound_ctrl:1
	v_add_f64 v[100:101], v[100:101], v[120:121]
	v_add_f64 v[102:103], v[102:103], v[122:123]
	v_add_f64 v[104:105], v[104:105], v[124:125]
	v_add_f64 v[106:107], v[106:107], v[126:127]
	v_add_f64 v[108:109], v[108:109], v[128:129]
	s_nop 1
	v_mov_b32_dpp v120, v100 quad_perm:[2,3,0,1] row_mask:0xf bank_mask:0xf bound_ctrl:1
	v_mov_b32_dpp v121, v101 quad_perm:[2,3,0,1] row_mask:0xf bank_mask:0xf bound_ctrl:1
	v_mov_b32_dpp v122, v102 quad_perm:[2,3,0,1] row_mask:0xf bank_mask:0xf bound_ctrl:1
	v_mov_b32_dpp v123, v103 quad_perm:[2,3,0,1] row_mask:0xf bank_mask:0xf bound_ctrl:1
	v_mov_b32_dpp v124, v104 quad_perm:[2,3,0,1] row_mask:0xf bank_mask:0xf bound_ctrl:1
	v_mov_b32_dpp v125, v105 quad_perm:[2,3,0,1] row_mask:0xf bank_mask:0xf bound_ctrl:1
	v_mov_b32_dpp v126, v106 quad_perm:[2,3,0,1] row_mask:0xf bank_mask:0xf bound_ctrl:1
	v_mov_b32_dpp v127, v107 quad_perm:[2,3,0,1] row_mask:0xf bank_mask:0xf bound_ctrl:1
	v_mov_b32_dpp v128, v108 quad_perm:[2,3,0,1] row_mask:0xf bank_mask:0xf bound_ctrl:1
	v_mov_b32_dpp v129, v109 quad_perm:[2,3,0,1] row_mask:0xf bank_mask:0xf bound_ctrl:1
	v_add_f64 v[100:101], v[100:101], v[120:121]
	v_add_f64 v[102:103], v[102:103], v[122:123]
	v_add_f64 v[104:105], v[104:105], v[124:125]
	v_add_f64 v[106:107], v[106:107], v[126:127]
	v_add_f64 v[108:109], v[108:109], v[128:129]
	s_nop 1
	v_mov_b32_dpp v120, v100 row_half_mirror row_mask:0xf bank_mask:0xf bound_ctrl:1
	v_mov_b32_dpp v121, v101 row_half_mirror row_mask:0xf bank_mask:0xf bound_ctrl:1
	v_mov_b32_dpp v122, v102 row_half_mirror row_mask:0xf bank_mask:0xf bound_ctrl:1
	v_mov_b32_dpp v123, v103 row_half_mirror row_mask:0xf bank_mask:0xf bound_ctrl:1
	v_mov_b32_dpp v124, v104 row_half_mirror row_mask:0xf bank_mask:0xf bound_ctrl:1
	v_mov_b32_dpp v125, v105 row_half_mirror row_mask:0xf bank_mask:0xf bound_ctrl:1
	v_mov_b32_dpp v126, v106 row_half_mirror row_mask:0xf bank_mask:0xf bound_ctrl:1
	v_mov_b32_dpp v127, v107 row_half_mirror row_mask:0xf bank_mask:0xf bound_ctrl:1
	v_mov_b32_dpp v128, v108 row_half_mirror row_mask:0xf bank_mask:0xf bound_ctrl:1
	v_mov_b32_dpp v129, v109 row_half_mirror row_mask:0xf bank_mask:0xf bound_ctrl:1
	v_add_f64 v[100:101], v[100:101], v[120:121]
	v_add_f64 v[102:103], v[102:103], v[122:123]
	v_add_f64 v[104:105], v[104:105], v[124:125]
	v_add_f64 v[106:107], v[106:107], v[126:127]
	v_add_f64 v[108:109], v[108:109], v[128:129]
	s_nop 1
	v_mov_b32_dpp v120, v100 row_mirror row_mask:0xf bank_mask:0xf bound_ctrl:1
	v_mov_b32_dpp v121, v101 row_mirror row_mask:0xf bank_mask:0xf bound_ctrl:1
	v_mov_b32_dpp v122, v102 row_mirror row_mask:0xf bank_mask:0xf bound_ctrl:1
	v_mov_b32_dpp v123, v103 row_mirror row_mask:0xf bank_mask:0xf bound_ctrl:1
	v_mov_b32_dpp v124, v104 row_mirror row_mask:0xf bank_mask:0xf bound_ctrl:1
	v_mov_b32_dpp v125, v105 row_mirror row_mask:0xf bank_mask:0xf bound_ctrl:1
	v_mov_b32_dpp v126, v106 row_mirror row_mask:0xf bank_mask:0xf bound_ctrl:1
	v_mov_b32_dpp v127, v107 row_mirror row_mask:0xf bank_mask:0xf bound_ctrl:1
	v_mov_b32_dpp v128, v108 row_mirror row_mask:0xf bank_mask:0xf bound_ctrl:1
	v_mov_b32_dpp v129, v109 row_mirror row_mask:0xf bank_mask:0xf bound_ctrl:1
	v_add_f64 v[100:101], v[100:101], v[120:121]
	v_add_f64 v[102:103], v[102:103], v[122:123]
	v_add_f64 v[104:105], v[104:105], v[124:125]
	v_add_f64 v[106:107], v[106:107], v[126:127]
	v_add_f64 v[108:109], v[108:109], v[128:129]
	s_nop 0
	v_readlane_b32 s70, v100, 0
	v_readlane_b32 s71, v101, 0
	v_readlane_b32 s72, v100, 16
	v_readlane_b32 s73, v101, 16
	v_readlane_b32 s74, v100, 32
	v_readlane_b32 s75, v101, 32
	v_readlane_b32 s76, v100, 48
	v_readlane_b32 s77, v101, 48
	v_mov_b32_e32 v130, s72
	v_mov_b32_e32 v131, s73
	v_mov_b32_e32 v132, s76
	v_mov_b32_e32 v133, s77
	v_add_f64 v[130:131], s[70:71], v[130:131]
	v_add_f64 v[132:133], s[74:75], v[132:133]
	v_add_f64 v[100:101], v[130:131], v[132:133]
	v_readlane_b32 s70, v102, 0
	v_readlane_b32 s71, v103, 0
	v_readlane_b32 s72, v102, 16
	v_readlane_b32 s73, v103, 16
	v_readlane_b32 s74, v102, 32
	v_readlane_b32 s75, v103, 32
	v_readlane_b32 s76, v102, 48
	v_readlane_b32 s77, v103, 48
	v_mov_b32_e32 v130, s72
	v_mov_b32_e32 v131, s73
	v_mov_b32_e32 v132, s76
	v_mov_b32_e32 v133, s77
	v_add_f64 v[130:131], s[70:71], v[130:131]
	v_add_f64 v[132:133], s[74:75], v[132:133]
	v_add_f64 v[102:103], v[130:131], v[132:133]
	v_readlane_b32 s70, v104, 0
	v_readlane_b32 s71, v105, 0
	v_readlane_b32 s72, v104, 16
	v_readlane_b32 s73, v105, 16
	v_readlane_b32 s74, v104, 32
	v_readlane_b32 s75, v105, 32
	v_readlane_b32 s76, v104, 48
	v_readlane_b32 s77, v105, 48
	v_mov_b32_e32 v130, s72
	v_mov_b32_e32 v131, s73
	v_mov_b32_e32 v132, s76
	v_mov_b32_e32 v133, s77
	v_add_f64 v[130:131], s[70:71], v[130:131]
	v_add_f64 v[132:133], s[74:75], v[132:133]
	v_add_f64 v[104:105], v[130:131], v[132:133]
	v_readlane_b32 s70, v106, 0
	v_readlane_b32 s71, v107, 0
	v_readlane_b32 s72, v106, 16
	v_readlane_b32 s73, v107, 16
	v_readlane_b32 s74, v106, 32
	v_readlane_b32 s75, v107, 32
	v_readlane_b32 s76, v106, 48
	v_readlane_b32 s77, v107, 48
	v_mov_b32_e32 v130, s72
	v_mov_b32_e32 v131, s73
	v_mov_b32_e32 v132, s76
	v_mov_b32_e32 v133, s77
	v_add_f64 v[130:131], s[70:71], v[130:131]
	v_add_f64 v[132:133], s[74:75], v[132:133]
	v_add_f64 v[106:107], v[130:131], v[132:133]
	v_readlane_b32 s70, v108, 0
	v_readlane_b32 s71, v109, 0
	v_readlane_b32 s72, v108, 16
	v_readlane_b32 s73, v109, 16
	v_readlane_b32 s74, v108, 32
	v_readlane_b32 s75, v109, 32
	v_readlane_b32 s76, v108, 48
	v_readlane_b32 s77, v109, 48
	v_mov_b32_e32 v130, s72
	v_mov_b32_e32 v131, s73
	v_mov_b32_e32 v132, s76
	v_mov_b32_e32 v133, s77
	v_add_f64 v[130:131], s[70:71], v[130:131]
	v_add_f64 v[132:133], s[74:75], v[132:133]
	v_add_f64 v[108:109], v[130:131], v[132:133]
	v_add_f64 v[104:105], v[100:101], v[104:105]
	v_fmac_f64_e32 v[104:105], -2.0, v[102:103]
	v_add_f64 v[108:109], v[100:101], v[108:109]
	v_fmac_f64_e32 v[108:109], -2.0, v[106:107]
	v_cvt_f32_f64_e32 v110, v[104:105]
	v_cvt_f32_f64_e32 v111, v[108:109]
	v_cmp_gt_f32_e32 vcc, v110, v111
	s_nop 1
	s_and_b64 s[68:69], vcc, exec
	s_cselect_b32 s8, s64, s61
	s_branch .LBB0_142
.Lslowc_1:
	s_or_b32 s19, s29, 1
	s_lshl_b32 s23, s19, 2
	s_add_i32 s23, s23, 0x11100
	v_mov_b32_e32 v4, s23
	ds_read_b32 v4, v4
	s_mulk_i32 s19, 0x810
	v_add_u32_e32 v8, s19, v135
	v_mov_b32_e32 v15, 0x7f800000
	s_waitcnt lgkmcnt(0)
	v_max_i32_e32 v4, 1, v4
	v_cvt_f64_u32_e32 v[12:13], v4
	v_div_scale_f64 v[16:17], s[30:31], v[12:13], v[12:13], 1.0
	v_rcp_f64_e32 v[20:21], v[16:17]
	v_div_scale_f64 v[22:23], vcc, 1.0, v[12:13], 1.0
	ds_read2st64_b64 v[4:7], v8 offset0:64 offset1:65
	ds_read2st64_b64 v[8:11], v8 offset0:66 offset1:67
	v_fma_f64 v[24:25], -v[16:17], v[20:21], 1.0
	v_fmac_f64_e32 v[20:21], v[20:21], v[24:25]
	v_fma_f64 v[24:25], -v[16:17], v[20:21], 1.0
	v_fmac_f64_e32 v[20:21], v[20:21], v[24:25]
	v_mul_f64 v[24:25], v[22:23], v[20:21]
	v_fma_f64 v[16:17], -v[16:17], v[24:25], v[22:23]
	v_div_fmas_f64 v[16:17], v[16:17], v[20:21], v[24:25]
	v_div_fixup_f64 v[12:13], v[16:17], v[12:13], 1.0
	s_waitcnt lgkmcnt(1)
	v_mul_f64 v[6:7], v[6:7], v[12:13]
	v_mul_f64 v[4:5], v[4:5], v[12:13]
	s_waitcnt lgkmcnt(0)
	v_mul_f64 v[8:9], v[8:9], v[12:13]
	v_mul_f64 v[10:11], v[12:13], v[10:11]
	v_mul_f64 v[12:13], v[6:7], v[6:7]
	v_fmac_f64_e32 v[12:13], v[4:5], v[4:5]
	v_fmac_f64_e32 v[12:13], v[8:9], v[8:9]
	v_fmac_f64_e32 v[12:13], v[10:11], v[10:11]
	s_nop 1
	v_mov_b32_dpp v16, v12 quad_perm:[1,0,3,2] row_mask:0xf bank_mask:0xf bound_ctrl:1
	v_mov_b32_dpp v17, v13 quad_perm:[1,0,3,2] row_mask:0xf bank_mask:0xf bound_ctrl:1
	v_add_f64 v[12:13], v[12:13], v[16:17]
	s_nop 1
	v_mov_b32_dpp v16, v12 quad_perm:[2,3,0,1] row_mask:0xf bank_mask:0xf bound_ctrl:1
	v_mov_b32_dpp v17, v13 quad_perm:[2,3,0,1] row_mask:0xf bank_mask:0xf bound_ctrl:1
	v_add_f64 v[12:13], v[12:13], v[16:17]
	s_nop 1
	v_mov_b32_dpp v16, v12 row_half_mirror row_mask:0xf bank_mask:0xf bound_ctrl:1
	v_mov_b32_dpp v17, v13 row_half_mirror row_mask:0xf bank_mask:0xf bound_ctrl:1
	v_add_f64 v[12:13], v[12:13], v[16:17]
	s_nop 1
	v_mov_b32_dpp v16, v12 row_mirror row_mask:0xf bank_mask:0xf bound_ctrl:1
	v_mov_b32_dpp v17, v13 row_mirror row_mask:0xf bank_mask:0xf bound_ctrl:1
	v_add_f64 v[12:13], v[12:13], v[16:17]
	s_nop 0
	v_readlane_b32 s19, v13, 16
	v_readlane_b32 s23, v12, 16
	v_readlane_b32 s31, v13, 0
	v_readlane_b32 s30, v12, 0
	v_mov_b32_e32 v16, s23
	v_mov_b32_e32 v17, s19
	v_readlane_b32 s19, v13, 48
	v_readlane_b32 s23, v12, 48
	v_add_f64 v[16:17], s[30:31], v[16:17]
	v_readlane_b32 s31, v13, 32
	v_readlane_b32 s30, v12, 32
	v_mov_b32_e32 v12, s23
	v_mov_b32_e32 v13, s19
	v_add_f64 v[12:13], s[30:31], v[12:13]
	v_add_f64 v[12:13], v[16:17], v[12:13]

.LBB0_142:
	s_mov_b32 s25, 0
	s_lshr_b64 s[26:27], s[6:7], 16
	s_and_b32 s24, s9, 0xffff
	s_and_b32 s26, s26, 0xffff0000
	s_mov_b32 s27, s25
	s_or_b64 s[26:27], s[26:27], s[24:25]
	s_and_b32 s31, s5, 0xffff
	s_mov_b32 s30, s25
	s_or_b64 s[26:27], s[26:27], s[30:31]
	s_lshl_b64 s[30:31], s[0:1], 16
	s_and_b32 s31, s31, 0xffff0000
	s_mov_b32 s30, s25
	s_or_b64 s[26:27], s[26:27], s[30:31]
	s_add_u32 s30, s26, -1
	s_addc_u32 s31, s27, -1
	s_and_b64 s[30:31], s[26:27], s[30:31]
	s_cmp_eq_u64 s[30:31], 0
	v_readlane_b32 s0, v14, 32
	s_cbranch_scc1 .LBB0_145
	s_bcnt1_i32_b64 s60, s[26:27]
	s_cmp_lg_u32 s60, 2
	s_cbranch_scc1 .Lslowc_2
	s_ff1_i32_b64 s61, s[26:27]
	s_mov_b64 s[62:63], s[26:27]
	s_bitset0_b64 s[62:63], s61
	s_ff1_i32_b64 s64, s[62:63]
	s_lshl_b32 s66, s61, 10
	s_mov_b32 s67, 0
	v_lshl_add_u64 v[66:67], v[2:3], 0, s[66:67]
	global_load_dwordx4 v[70:73], v[66:67], off
	s_lshl_b32 s66, s64, 10
	v_lshl_add_u64 v[68:69], v[2:3], 0, s[66:67]
	global_load_dwordx4 v[74:77], v[68:69], off
	s_add_i32 s65, s29, 2
	s_lshl_b32 s66, s65, 2
	s_add_i32 s66, s66, 0x11100
	v_mov_b32_e32 v78, s66
	ds_read_b32 v78, v78
	s_mul_i32 s66, s65, 0x810
	v_add_u32_e32 v79, s66, v135
	ds_read2st64_b64 v[80:83], v79 offset0:64 offset1:65
	ds_read2st64_b64 v[84:87], v79 offset0:66 offset1:67
	s_waitcnt lgkmcnt(2)
	v_max_i32_e32 v78, 1, v78
	v_cvt_f64_u32_e32 v[88:89], v78
	v_div_scale_f64 v[90:91], s[68:69], v[88:89], v[88:89], 1.0
	v_rcp_f64_e32 v[92:93], v[90:91]
	v_div_scale_f64 v[94:95], vcc, 1.0, v[88:89], 1.0
	v_fma_f64 v[96:97], -v[90:91], v[92:93], 1.0
	v_fmac_f64_e32 v[92:93], v[92:93], v[96:97]
	v_fma_f64 v[96:97], -v[90:91], v[92:93], 1.0
	v_fmac_f64_e32 v[92:93], v[92:93], v[96:97]
	v_mul_f64 v[96:97], v[94:95], v[92:93]
	v_fma_f64 v[90:91], -v[90:91], v[96:97], v[94:95]
	v_div_fmas_f64 v[90:91], v[90:91], v[92:93], v[96:97]
	v_div_fixup_f64 v[88:89], v[90:91], v[88:89], 1.0
	s_waitcnt lgkmcnt(0)
	v_mul_f64 v[82:83], v[82:83], v[88:89]
	v_mul_f64 v[80:81], v[80:81], v[88:89]
	v_mul_f64 v[84:85], v[84:85], v[88:89]
	v_mul_f64 v[86:87], v[88:89], v[86:87]
	v_mul_f64 v[100:101], v[82:83], v[82:83]
	v_fmac_f64_e32 v[100:101], v[80:81], v[80:81]
	v_fmac_f64_e32 v[100:101], v[84:85], v[84:85]
	v_fmac_f64_e32 v[100:101], v[86:87], v[86:87]
	s_waitcnt vmcnt(0)
	v_cvt_f64_f32_e32 v[110:111], v70
	v_cvt_f64_f32_e32 v[112:113], v71
	v_cvt_f64_f32_e32 v[114:115], v72
	v_cvt_f64_f32_e32 v[116:117], v73
	v_mul_f64 v[102:103], v[82:83], v[112:113]
	v_mul_f64 v[104:105], v[112:113], v[112:113]
	v_fmac_f64_e32 v[102:103], v[80:81], v[110:111]
	v_fmac_f64_e32 v[104:105], v[110:111], v[110:111]
	v_fmac_f64_e32 v[102:103], v[84:85], v[114:115]
	v_fmac_f64_e32 v[104:105], v[114:115], v[114:115]
	v_fmac_f64_e32 v[102:103], v[86:87], v[116:117]
	v_fmac_f64_e32 v[104:105], v[116:117], v[116:117]
	v_cvt_f64_f32_e32 v[110:111], v74
	v_cvt_f64_f32_e32 v[112:113], v75
	v_cvt_f64_f32_e32 v[114:115], v76
	v_cvt_f64_f32_e32 v[116:117], v77
	v_mul_f64 v[106:107], v[82:83], v[112:113]
	v_mul_f64 v[108:109], v[112:113], v[112:113]
	v_fmac_f64_e32 v[106:107], v[80:81], v[110:111]
	v_fmac_f64_e32 v[108:109], v[110:111], v[110:111]
	v_fmac_f64_e32 v[106:107], v[84:85], v[114:115]
	v_fmac_f64_e32 v[108:109], v[114:115], v[114:115]
	v_fmac_f64_e32 v[106:107], v[86:87], v[116:117]
	v_fmac_f64_e32 v[108:109], v[116:117], v[116:117]
	s_nop 1
	v_mov_b32_dpp v120, v100 quad_perm:[1,0,3,2] row_mask:0xf bank_mask:0xf bound_ctrl:1
	v_mov_b32_dpp v121, v101 quad_perm:[1,0,3,2] row_mask:0xf bank_mask:0xf bound_ctrl:1
	v_mov_b32_dpp v122, v102 quad_perm:[1,0,3,2] row_mask:0xf bank_mask:0xf bound_ctrl:1
	v_mov_b32_dpp v123, v103 quad_perm:[1,0,3,2] row_mask:0xf bank_mask:0xf bound_ctrl:1
	v_mov_b32_dpp v124, v104 quad_perm:[1,0,3,2] row_mask:0xf bank_mask:0xf bound_ctrl:1
	v_mov_b32_dpp v125, v105 quad_perm:[1,0,3,2] row_mask:0xf bank_mask:0xf bound_ctrl:1
	v_mov_b32_dpp v126, v106 quad_perm:[1,0,3,2] row_mask:0xf bank_mask:0xf bound_ctrl:1
	v_mov_b32_dpp v127, v107 quad_perm:[1,0,3,2] row_mask:0xf bank_mask:0xf bound_ctrl:1
	v_mov_b32_dpp v128, v108 quad_perm:[1,0,3,2] row_mask:0xf bank_mask:0xf bound_ctrl:1
	v_mov_b32_dpp v129, v109 quad_perm:[1,0,3,2] row_mask:0xf bank_mask:0xf bound_ctrl:1
	v_add_f64 v[100:101], v[100:101], v[120:121]
	v_add_f64 v[102:103], v[102:103], v[122:123]
	v_add_f64 v[104:105], v[104:105], v[124:125]
	v_add_f64 v[106:107], v[106:107], v[126:127]
	v_add_f64 v[108:109], v[108:109], v[128:129]
	s_nop 1
	v_mov_b32_dpp v120, v100 quad_perm:[2,3,0,1] row_mask:0xf bank_mask:0xf bound_ctrl:1
	v_mov_b32_dpp v121, v101 quad_perm:[2,3,0,1] row_mask:0xf bank_mask:0xf bound_ctrl:1
	v_mov_b32_dpp v122, v102 quad_perm:[2,3,0,1] row_mask:0xf bank_mask:0xf bound_ctrl:1
	v_mov_b32_dpp v123, v103 quad_perm:[2,3,0,1] row_mask:0xf bank_mask:0xf bound_ctrl:1
	v_mov_b32_dpp v124, v104 quad_perm:[2,3,0,1] row_mask:0xf bank_mask:0xf bound_ctrl:1
	v_mov_b32_dpp v125, v105 quad_perm:[2,3,0,1] row_mask:0xf bank_mask:0xf bound_ctrl:1
	v_mov_b32_dpp v126, v106 quad_perm:[2,3,0,1] row_mask:0xf bank_mask:0xf bound_ctrl:1
	v_mov_b32_dpp v127, v107 quad_perm:[2,3,0,1] row_mask:0xf bank_mask:0xf bound_ctrl:1
	v_mov_b32_dpp v128, v108 quad_perm:[2,3,0,1] row_mask:0xf bank_mask:0xf bound_ctrl:1
	v_mov_b32_dpp v129, v109 quad_perm:[2,3,0,1] row_mask:0xf bank_mask:0xf bound_ctrl:1
	v_add_f64 v[100:101], v[100:101], v[120:121]
	v_add_f64 v[102:103], v[102:103], v[122:123]
	v_add_f64 v[104:105], v[104:105], v[124:125]
	v_add_f64 v[106:107], v[106:107], v[126:127]
	v_add_f64 v[108:109], v[108:109], v[128:129]
	s_nop 1
	v_mov_b32_dpp v120, v100 row_half_mirror row_mask:0xf bank_mask:0xf bound_ctrl:1
	v_mov_b32_dpp v121, v101 row_half_mirror row_mask:0xf bank_mask:0xf bound_ctrl:1
	v_mov_b32_dpp v122, v102 row_half_mirror row_mask:0xf bank_mask:0xf bound_ctrl:1
	v_mov_b32_dpp v123, v103 row_half_mirror row_mask:0xf bank_mask:0xf bound_ctrl:1
	v_mov_b32_dpp v124, v104 row_half_mirror row_mask:0xf bank_mask:0xf bound_ctrl:1
	v_mov_b32_dpp v125, v105 row_half_mirror row_mask:0xf bank_mask:0xf bound_ctrl:1
	v_mov_b32_dpp v126, v106 row_half_mirror row_mask:0xf bank_mask:0xf bound_ctrl:1
	v_mov_b32_dpp v127, v107 row_half_mirror row_mask:0xf bank_mask:0xf bound_ctrl:1
	v_mov_b32_dpp v128, v108 row_half_mirror row_mask:0xf bank_mask:0xf bound_ctrl:1
	v_mov_b32_dpp v129, v109 row_half_mirror row_mask:0xf bank_mask:0xf bound_ctrl:1
	v_add_f64 v[100:101], v[100:101], v[120:121]
	v_add_f64 v[102:103], v[102:103], v[122:123]
	v_add_f64 v[104:105], v[104:105], v[124:125]
	v_add_f64 v[106:107], v[106:107], v[126:127]
	v_add_f64 v[108:109], v[108:109], v[128:129]
	s_nop 1
	v_mov_b32_dpp v120, v100 row_mirror row_mask:0xf bank_mask:0xf bound_ctrl:1
	v_mov_b32_dpp v121, v101 row_mirror row_mask:0xf bank_mask:0xf bound_ctrl:1
	v_mov_b32_dpp v122, v102 row_mirror row_mask:0xf bank_mask:0xf bound_ctrl:1
	v_mov_b32_dpp v123, v103 row_mirror row_mask:0xf bank_mask:0xf bound_ctrl:1
	v_mov_b32_dpp v124, v104 row_mirror row_mask:0xf bank_mask:0xf bound_ctrl:1
	v_mov_b32_dpp v125, v105 row_mirror row_mask:0xf bank_mask:0xf bound_ctrl:1
	v_mov_b32_dpp v126, v106 row_mirror row_mask:0xf bank_mask:0xf bound_ctrl:1
	v_mov_b32_dpp v127, v107 row_mirror row_mask:0xf bank_mask:0xf bound_ctrl:1
	v_mov_b32_dpp v128, v108 row_mirror row_mask:0xf bank_mask:0xf bound_ctrl:1
	v_mov_b32_dpp v129, v109 row_mirror row_mask:0xf bank_mask:0xf bound_ctrl:1
	v_add_f64 v[100:101], v[100:101], v[120:121]
	v_add_f64 v[102:103], v[102:103], v[122:123]
	v_add_f64 v[104:105], v[104:105], v[124:125]
	v_add_f64 v[106:107], v[106:107], v[126:127]
	v_add_f64 v[108:109], v[108:109], v[128:129]
	s_nop 0
	v_readlane_b32 s70, v100, 0
	v_readlane_b32 s71, v101, 0
	v_readlane_b32 s72, v100, 16
	v_readlane_b32 s73, v101, 16
	v_readlane_b32 s74, v100, 32
	v_readlane_b32 s75, v101, 32
	v_readlane_b32 s76, v100, 48
	v_readlane_b32 s77, v101, 48
	v_mov_b32_e32 v130, s72
	v_mov_b32_e32 v131, s73
	v_mov_b32_e32 v132, s76
	v_mov_b32_e32 v133, s77
	v_add_f64 v[130:131], s[70:71], v[130:131]
	v_add_f64 v[132:133], s[74:75], v[132:133]
	v_add_f64 v[100:101], v[130:131], v[132:133]
	v_readlane_b32 s70, v102, 0
	v_readlane_b32 s71, v103, 0
	v_readlane_b32 s72, v102, 16
	v_readlane_b32 s73, v103, 16
	v_readlane_b32 s74, v102, 32
	v_readlane_b32 s75, v103, 32
	v_readlane_b32 s76, v102, 48
	v_readlane_b32 s77, v103, 48
	v_mov_b32_e32 v130, s72
	v_mov_b32_e32 v131, s73
	v_mov_b32_e32 v132, s76
	v_mov_b32_e32 v133, s77
	v_add_f64 v[130:131], s[70:71], v[130:131]
	v_add_f64 v[132:133], s[74:75], v[132:133]
	v_add_f64 v[102:103], v[130:131], v[132:133]
	v_readlane_b32 s70, v104, 0
	v_readlane_b32 s71, v105, 0
	v_readlane_b32 s72, v104, 16
	v_readlane_b32 s73, v105, 16
	v_readlane_b32 s74, v104, 32
	v_readlane_b32 s75, v105, 32
	v_readlane_b32 s76, v104, 48
	v_readlane_b32 s77, v105, 48
	v_mov_b32_e32 v130, s72
	v_mov_b32_e32 v131, s73
	v_mov_b32_e32 v132, s76
	v_mov_b32_e32 v133, s77
	v_add_f64 v[130:131], s[70:71], v[130:131]
	v_add_f64 v[132:133], s[74:75], v[132:133]
	v_add_f64 v[104:105], v[130:131], v[132:133]
	v_readlane_b32 s70, v106, 0
	v_readlane_b32 s71, v107, 0
	v_readlane_b32 s72, v106, 16
	v_readlane_b32 s73, v107, 16
	v_readlane_b32 s74, v106, 32
	v_readlane_b32 s75, v107, 32
	v_readlane_b32 s76, v106, 48
	v_readlane_b32 s77, v107, 48
	v_mov_b32_e32 v130, s72
	v_mov_b32_e32 v131, s73
	v_mov_b32_e32 v132, s76
	v_mov_b32_e32 v133, s77
	v_add_f64 v[130:131], s[70:71], v[130:131]
	v_add_f64 v[132:133], s[74:75], v[132:133]
	v_add_f64 v[106:107], v[130:131], v[132:133]
	v_readlane_b32 s70, v108, 0
	v_readlane_b32 s71, v109, 0
	v_readlane_b32 s72, v108, 16
	v_readlane_b32 s73, v109, 16
	v_readlane_b32 s74, v108, 32
	v_readlane_b32 s75, v109, 32
	v_readlane_b32 s76, v108, 48
	v_readlane_b32 s77, v109, 48
	v_mov_b32_e32 v130, s72
	v_mov_b32_e32 v131, s73
	v_mov_b32_e32 v132, s76
	v_mov_b32_e32 v133, s77
	v_add_f64 v[130:131], s[70:71], v[130:131]
	v_add_f64 v[132:133], s[74:75], v[132:133]
	v_add_f64 v[108:109], v[130:131], v[132:133]
	v_add_f64 v[104:105], v[100:101], v[104:105]
	v_fmac_f64_e32 v[104:105], -2.0, v[102:103]
	v_add_f64 v[108:109], v[100:101], v[108:109]
	v_fmac_f64_e32 v[108:109], -2.0, v[106:107]
	v_cvt_f32_f64_e32 v110, v[104:105]
	v_cvt_f32_f64_e32 v111, v[108:109]
	v_cmp_gt_f32_e32 vcc, v110, v111
	s_nop 1
	s_and_b64 s[68:69], vcc, exec
	s_cselect_b32 s0, s64, s61
	s_branch .LBB0_145
.Lslowc_2:
	s_or_b32 s6, s29, 2
	s_lshl_b32 s19, s6, 2
	s_add_i32 s19, s19, 0x11100
	v_mov_b32_e32 v4, s19
	ds_read_b32 v4, v4
	s_mulk_i32 s6, 0x810
	v_add_u32_e32 v8, s6, v135
	v_mov_b32_e32 v15, 0x7f800000
	s_waitcnt lgkmcnt(0)
	v_max_i32_e32 v4, 1, v4
	v_cvt_f64_u32_e32 v[12:13], v4
	v_div_scale_f64 v[16:17], s[30:31], v[12:13], v[12:13], 1.0
	v_rcp_f64_e32 v[20:21], v[16:17]
	v_div_scale_f64 v[22:23], vcc, 1.0, v[12:13], 1.0
	ds_read2st64_b64 v[4:7], v8 offset0:64 offset1:65
	ds_read2st64_b64 v[8:11], v8 offset0:66 offset1:67
	v_fma_f64 v[24:25], -v[16:17], v[20:21], 1.0
	v_fmac_f64_e32 v[20:21], v[20:21], v[24:25]
	v_fma_f64 v[24:25], -v[16:17], v[20:21], 1.0
	v_fmac_f64_e32 v[20:21], v[20:21], v[24:25]
	v_mul_f64 v[24:25], v[22:23], v[20:21]
	v_fma_f64 v[16:17], -v[16:17], v[24:25], v[22:23]
	v_div_fmas_f64 v[16:17], v[16:17], v[20:21], v[24:25]
	v_div_fixup_f64 v[12:13], v[16:17], v[12:13], 1.0
	s_waitcnt lgkmcnt(1)
	v_mul_f64 v[6:7], v[6:7], v[12:13]
	v_mul_f64 v[4:5], v[4:5], v[12:13]
	s_waitcnt lgkmcnt(0)
	v_mul_f64 v[8:9], v[8:9], v[12:13]
	v_mul_f64 v[10:11], v[12:13], v[10:11]
	v_mul_f64 v[12:13], v[6:7], v[6:7]
	v_fmac_f64_e32 v[12:13], v[4:5], v[4:5]
	v_fmac_f64_e32 v[12:13], v[8:9], v[8:9]
	v_fmac_f64_e32 v[12:13], v[10:11], v[10:11]
	s_nop 1
	v_mov_b32_dpp v16, v12 quad_perm:[1,0,3,2] row_mask:0xf bank_mask:0xf bound_ctrl:1
	v_mov_b32_dpp v17, v13 quad_perm:[1,0,3,2] row_mask:0xf bank_mask:0xf bound_ctrl:1
	v_add_f64 v[12:13], v[12:13], v[16:17]
	s_nop 1
	v_mov_b32_dpp v16, v12 quad_perm:[2,3,0,1] row_mask:0xf bank_mask:0xf bound_ctrl:1
	v_mov_b32_dpp v17, v13 quad_perm:[2,3,0,1] row_mask:0xf bank_mask:0xf bound_ctrl:1
	v_add_f64 v[12:13], v[12:13], v[16:17]
	s_nop 1
	v_mov_b32_dpp v16, v12 row_half_mirror row_mask:0xf bank_mask:0xf bound_ctrl:1
	v_mov_b32_dpp v17, v13 row_half_mirror row_mask:0xf bank_mask:0xf bound_ctrl:1
	v_add_f64 v[12:13], v[12:13], v[16:17]
	s_nop 1
	v_mov_b32_dpp v16, v12 row_mirror row_mask:0xf bank_mask:0xf bound_ctrl:1
	v_mov_b32_dpp v17, v13 row_mirror row_mask:0xf bank_mask:0xf bound_ctrl:1
	v_add_f64 v[12:13], v[12:13], v[16:17]
	s_nop 0
	v_readlane_b32 s6, v13, 16
	v_readlane_b32 s19, v12, 16
	v_readlane_b32 s31, v13, 0
	v_readlane_b32 s30, v12, 0
	v_mov_b32_e32 v16, s19
	v_mov_b32_e32 v17, s6
	v_readlane_b32 s6, v13, 48
	v_readlane_b32 s19, v12, 48
	v_add_f64 v[16:17], s[30:31], v[16:17]
	v_readlane_b32 s31, v13, 32
	v_readlane_b32 s30, v12, 32
	v_mov_b32_e32 v12, s19
	v_mov_b32_e32 v13, s6
	v_add_f64 v[12:13], s[30:31], v[12:13]
	v_add_f64 v[12:13], v[16:17], v[12:13]

.LBB0_145:
	s_mov_b32 s25, 0
	s_lshr_b32 s24, s9, 16
	s_and_b32 s6, s7, 0xffff0000
	s_mov_b32 s7, s25
	s_lshr_b64 s[4:5], s[4:5], 16
	s_or_b64 s[6:7], s[6:7], s[24:25]
	s_mov_b32 s4, s25
	s_or_b64 s[4:5], s[6:7], s[4:5]
	s_and_b32 s7, s1, 0xffff0000
	s_mov_b32 s6, s25
	s_or_b64 s[6:7], s[4:5], s[6:7]
	s_add_u32 s4, s6, -1
	s_addc_u32 s5, s7, -1
	s_and_b64 s[4:5], s[6:7], s[4:5]
	s_cmp_eq_u64 s[4:5], 0
	v_readlane_b32 s4, v14, 48
	s_cbranch_scc1 .LBB0_148
	s_bcnt1_i32_b64 s60, s[6:7]
	s_cmp_lg_u32 s60, 2
	s_cbranch_scc1 .Lslowc_3
	s_ff1_i32_b64 s61, s[6:7]
	s_mov_b64 s[62:63], s[6:7]
	s_bitset0_b64 s[62:63], s61
	s_ff1_i32_b64 s64, s[62:63]
	s_lshl_b32 s66, s61, 10
	s_mov_b32 s67, 0
	v_lshl_add_u64 v[66:67], v[2:3], 0, s[66:67]
	global_load_dwordx4 v[70:73], v[66:67], off
	s_lshl_b32 s66, s64, 10
	v_lshl_add_u64 v[68:69], v[2:3], 0, s[66:67]
	global_load_dwordx4 v[74:77], v[68:69], off
	s_add_i32 s65, s29, 3
	s_lshl_b32 s66, s65, 2
	s_add_i32 s66, s66, 0x11100
	v_mov_b32_e32 v78, s66
	ds_read_b32 v78, v78
	s_mul_i32 s66, s65, 0x810
	v_add_u32_e32 v79, s66, v135
	ds_read2st64_b64 v[80:83], v79 offset0:64 offset1:65
	ds_read2st64_b64 v[84:87], v79 offset0:66 offset1:67
	s_waitcnt lgkmcnt(2)
	v_max_i32_e32 v78, 1, v78
	v_cvt_f64_u32_e32 v[88:89], v78
	v_div_scale_f64 v[90:91], s[68:69], v[88:89], v[88:89], 1.0
	v_rcp_f64_e32 v[92:93], v[90:91]
	v_div_scale_f64 v[94:95], vcc, 1.0, v[88:89], 1.0
	v_fma_f64 v[96:97], -v[90:91], v[92:93], 1.0
	v_fmac_f64_e32 v[92:93], v[92:93], v[96:97]
	v_fma_f64 v[96:97], -v[90:91], v[92:93], 1.0
	v_fmac_f64_e32 v[92:93], v[92:93], v[96:97]
	v_mul_f64 v[96:97], v[94:95], v[92:93]
	v_fma_f64 v[90:91], -v[90:91], v[96:97], v[94:95]
	v_div_fmas_f64 v[90:91], v[90:91], v[92:93], v[96:97]
	v_div_fixup_f64 v[88:89], v[90:91], v[88:89], 1.0
	s_waitcnt lgkmcnt(0)
	v_mul_f64 v[82:83], v[82:83], v[88:89]
	v_mul_f64 v[80:81], v[80:81], v[88:89]
	v_mul_f64 v[84:85], v[84:85], v[88:89]
	v_mul_f64 v[86:87], v[88:89], v[86:87]
	v_mul_f64 v[100:101], v[82:83], v[82:83]
	v_fmac_f64_e32 v[100:101], v[80:81], v[80:81]
	v_fmac_f64_e32 v[100:101], v[84:85], v[84:85]
	v_fmac_f64_e32 v[100:101], v[86:87], v[86:87]
	s_waitcnt vmcnt(0)
	v_cvt_f64_f32_e32 v[110:111], v70
	v_cvt_f64_f32_e32 v[112:113], v71
	v_cvt_f64_f32_e32 v[114:115], v72
	v_cvt_f64_f32_e32 v[116:117], v73
	v_mul_f64 v[102:103], v[82:83], v[112:113]
	v_mul_f64 v[104:105], v[112:113], v[112:113]
	v_fmac_f64_e32 v[102:103], v[80:81], v[110:111]
	v_fmac_f64_e32 v[104:105], v[110:111], v[110:111]
	v_fmac_f64_e32 v[102:103], v[84:85], v[114:115]
	v_fmac_f64_e32 v[104:105], v[114:115], v[114:115]
	v_fmac_f64_e32 v[102:103], v[86:87], v[116:117]
	v_fmac_f64_e32 v[104:105], v[116:117], v[116:117]
	v_cvt_f64_f32_e32 v[110:111], v74
	v_cvt_f64_f32_e32 v[112:113], v75
	v_cvt_f64_f32_e32 v[114:115], v76
	v_cvt_f64_f32_e32 v[116:117], v77
	v_mul_f64 v[106:107], v[82:83], v[112:113]
	v_mul_f64 v[108:109], v[112:113], v[112:113]
	v_fmac_f64_e32 v[106:107], v[80:81], v[110:111]
	v_fmac_f64_e32 v[108:109], v[110:111], v[110:111]
	v_fmac_f64_e32 v[106:107], v[84:85], v[114:115]
	v_fmac_f64_e32 v[108:109], v[114:115], v[114:115]
	v_fmac_f64_e32 v[106:107], v[86:87], v[116:117]
	v_fmac_f64_e32 v[108:109], v[116:117], v[116:117]
	s_nop 1
	v_mov_b32_dpp v120, v100 quad_perm:[1,0,3,2] row_mask:0xf bank_mask:0xf bound_ctrl:1
	v_mov_b32_dpp v121, v101 quad_perm:[1,0,3,2] row_mask:0xf bank_mask:0xf bound_ctrl:1
	v_mov_b32_dpp v122, v102 quad_perm:[1,0,3,2] row_mask:0xf bank_mask:0xf bound_ctrl:1
	v_mov_b32_dpp v123, v103 quad_perm:[1,0,3,2] row_mask:0xf bank_mask:0xf bound_ctrl:1
	v_mov_b32_dpp v124, v104 quad_perm:[1,0,3,2] row_mask:0xf bank_mask:0xf bound_ctrl:1
	v_mov_b32_dpp v125, v105 quad_perm:[1,0,3,2] row_mask:0xf bank_mask:0xf bound_ctrl:1
	v_mov_b32_dpp v126, v106 quad_perm:[1,0,3,2] row_mask:0xf bank_mask:0xf bound_ctrl:1
	v_mov_b32_dpp v127, v107 quad_perm:[1,0,3,2] row_mask:0xf bank_mask:0xf bound_ctrl:1
	v_mov_b32_dpp v128, v108 quad_perm:[1,0,3,2] row_mask:0xf bank_mask:0xf bound_ctrl:1
	v_mov_b32_dpp v129, v109 quad_perm:[1,0,3,2] row_mask:0xf bank_mask:0xf bound_ctrl:1
	v_add_f64 v[100:101], v[100:101], v[120:121]
	v_add_f64 v[102:103], v[102:103], v[122:123]
	v_add_f64 v[104:105], v[104:105], v[124:125]
	v_add_f64 v[106:107], v[106:107], v[126:127]
	v_add_f64 v[108:109], v[108:109], v[128:129]
	s_nop 1
	v_mov_b32_dpp v120, v100 quad_perm:[2,3,0,1] row_mask:0xf bank_mask:0xf bound_ctrl:1
	v_mov_b32_dpp v121, v101 quad_perm:[2,3,0,1] row_mask:0xf bank_mask:0xf bound_ctrl:1
	v_mov_b32_dpp v122, v102 quad_perm:[2,3,0,1] row_mask:0xf bank_mask:0xf bound_ctrl:1
	v_mov_b32_dpp v123, v103 quad_perm:[2,3,0,1] row_mask:0xf bank_mask:0xf bound_ctrl:1
	v_mov_b32_dpp v124, v104 quad_perm:[2,3,0,1] row_mask:0xf bank_mask:0xf bound_ctrl:1
	v_mov_b32_dpp v125, v105 quad_perm:[2,3,0,1] row_mask:0xf bank_mask:0xf bound_ctrl:1
	v_mov_b32_dpp v126, v106 quad_perm:[2,3,0,1] row_mask:0xf bank_mask:0xf bound_ctrl:1
	v_mov_b32_dpp v127, v107 quad_perm:[2,3,0,1] row_mask:0xf bank_mask:0xf bound_ctrl:1
	v_mov_b32_dpp v128, v108 quad_perm:[2,3,0,1] row_mask:0xf bank_mask:0xf bound_ctrl:1
	v_mov_b32_dpp v129, v109 quad_perm:[2,3,0,1] row_mask:0xf bank_mask:0xf bound_ctrl:1
	v_add_f64 v[100:101], v[100:101], v[120:121]
	v_add_f64 v[102:103], v[102:103], v[122:123]
	v_add_f64 v[104:105], v[104:105], v[124:125]
	v_add_f64 v[106:107], v[106:107], v[126:127]
	v_add_f64 v[108:109], v[108:109], v[128:129]
	s_nop 1
	v_mov_b32_dpp v120, v100 row_half_mirror row_mask:0xf bank_mask:0xf bound_ctrl:1
	v_mov_b32_dpp v121, v101 row_half_mirror row_mask:0xf bank_mask:0xf bound_ctrl:1
	v_mov_b32_dpp v122, v102 row_half_mirror row_mask:0xf bank_mask:0xf bound_ctrl:1
	v_mov_b32_dpp v123, v103 row_half_mirror row_mask:0xf bank_mask:0xf bound_ctrl:1
	v_mov_b32_dpp v124, v104 row_half_mirror row_mask:0xf bank_mask:0xf bound_ctrl:1
	v_mov_b32_dpp v125, v105 row_half_mirror row_mask:0xf bank_mask:0xf bound_ctrl:1
	v_mov_b32_dpp v126, v106 row_half_mirror row_mask:0xf bank_mask:0xf bound_ctrl:1
	v_mov_b32_dpp v127, v107 row_half_mirror row_mask:0xf bank_mask:0xf bound_ctrl:1
	v_mov_b32_dpp v128, v108 row_half_mirror row_mask:0xf bank_mask:0xf bound_ctrl:1
	v_mov_b32_dpp v129, v109 row_half_mirror row_mask:0xf bank_mask:0xf bound_ctrl:1
	v_add_f64 v[100:101], v[100:101], v[120:121]
	v_add_f64 v[102:103], v[102:103], v[122:123]
	v_add_f64 v[104:105], v[104:105], v[124:125]
	v_add_f64 v[106:107], v[106:107], v[126:127]
	v_add_f64 v[108:109], v[108:109], v[128:129]
	s_nop 1
	v_mov_b32_dpp v120, v100 row_mirror row_mask:0xf bank_mask:0xf bound_ctrl:1
	v_mov_b32_dpp v121, v101 row_mirror row_mask:0xf bank_mask:0xf bound_ctrl:1
	v_mov_b32_dpp v122, v102 row_mirror row_mask:0xf bank_mask:0xf bound_ctrl:1
	v_mov_b32_dpp v123, v103 row_mirror row_mask:0xf bank_mask:0xf bound_ctrl:1
	v_mov_b32_dpp v124, v104 row_mirror row_mask:0xf bank_mask:0xf bound_ctrl:1
	v_mov_b32_dpp v125, v105 row_mirror row_mask:0xf bank_mask:0xf bound_ctrl:1
	v_mov_b32_dpp v126, v106 row_mirror row_mask:0xf bank_mask:0xf bound_ctrl:1
	v_mov_b32_dpp v127, v107 row_mirror row_mask:0xf bank_mask:0xf bound_ctrl:1
	v_mov_b32_dpp v128, v108 row_mirror row_mask:0xf bank_mask:0xf bound_ctrl:1
	v_mov_b32_dpp v129, v109 row_mirror row_mask:0xf bank_mask:0xf bound_ctrl:1
	v_add_f64 v[100:101], v[100:101], v[120:121]
	v_add_f64 v[102:103], v[102:103], v[122:123]
	v_add_f64 v[104:105], v[104:105], v[124:125]
	v_add_f64 v[106:107], v[106:107], v[126:127]
	v_add_f64 v[108:109], v[108:109], v[128:129]
	s_nop 0
	v_readlane_b32 s70, v100, 0
	v_readlane_b32 s71, v101, 0
	v_readlane_b32 s72, v100, 16
	v_readlane_b32 s73, v101, 16
	v_readlane_b32 s74, v100, 32
	v_readlane_b32 s75, v101, 32
	v_readlane_b32 s76, v100, 48
	v_readlane_b32 s77, v101, 48
	v_mov_b32_e32 v130, s72
	v_mov_b32_e32 v131, s73
	v_mov_b32_e32 v132, s76
	v_mov_b32_e32 v133, s77
	v_add_f64 v[130:131], s[70:71], v[130:131]
	v_add_f64 v[132:133], s[74:75], v[132:133]
	v_add_f64 v[100:101], v[130:131], v[132:133]
	v_readlane_b32 s70, v102, 0
	v_readlane_b32 s71, v103, 0
	v_readlane_b32 s72, v102, 16
	v_readlane_b32 s73, v103, 16
	v_readlane_b32 s74, v102, 32
	v_readlane_b32 s75, v103, 32
	v_readlane_b32 s76, v102, 48
	v_readlane_b32 s77, v103, 48
	v_mov_b32_e32 v130, s72
	v_mov_b32_e32 v131, s73
	v_mov_b32_e32 v132, s76
	v_mov_b32_e32 v133, s77
	v_add_f64 v[130:131], s[70:71], v[130:131]
	v_add_f64 v[132:133], s[74:75], v[132:133]
	v_add_f64 v[102:103], v[130:131], v[132:133]
	v_readlane_b32 s70, v104, 0
	v_readlane_b32 s71, v105, 0
	v_readlane_b32 s72, v104, 16
	v_readlane_b32 s73, v105, 16
	v_readlane_b32 s74, v104, 32
	v_readlane_b32 s75, v105, 32
	v_readlane_b32 s76, v104, 48
	v_readlane_b32 s77, v105, 48
	v_mov_b32_e32 v130, s72
	v_mov_b32_e32 v131, s73
	v_mov_b32_e32 v132, s76
	v_mov_b32_e32 v133, s77
	v_add_f64 v[130:131], s[70:71], v[130:131]
	v_add_f64 v[132:133], s[74:75], v[132:133]
	v_add_f64 v[104:105], v[130:131], v[132:133]
	v_readlane_b32 s70, v106, 0
	v_readlane_b32 s71, v107, 0
	v_readlane_b32 s72, v106, 16
	v_readlane_b32 s73, v107, 16
	v_readlane_b32 s74, v106, 32
	v_readlane_b32 s75, v107, 32
	v_readlane_b32 s76, v106, 48
	v_readlane_b32 s77, v107, 48
	v_mov_b32_e32 v130, s72
	v_mov_b32_e32 v131, s73
	v_mov_b32_e32 v132, s76
	v_mov_b32_e32 v133, s77
	v_add_f64 v[130:131], s[70:71], v[130:131]
	v_add_f64 v[132:133], s[74:75], v[132:133]
	v_add_f64 v[106:107], v[130:131], v[132:133]
	v_readlane_b32 s70, v108, 0
	v_readlane_b32 s71, v109, 0
	v_readlane_b32 s72, v108, 16
	v_readlane_b32 s73, v109, 16
	v_readlane_b32 s74, v108, 32
	v_readlane_b32 s75, v109, 32
	v_readlane_b32 s76, v108, 48
	v_readlane_b32 s77, v109, 48
	v_mov_b32_e32 v130, s72
	v_mov_b32_e32 v131, s73
	v_mov_b32_e32 v132, s76
	v_mov_b32_e32 v133, s77
	v_add_f64 v[130:131], s[70:71], v[130:131]
	v_add_f64 v[132:133], s[74:75], v[132:133]
	v_add_f64 v[108:109], v[130:131], v[132:133]
	v_add_f64 v[104:105], v[100:101], v[104:105]
	v_fmac_f64_e32 v[104:105], -2.0, v[102:103]
	v_add_f64 v[108:109], v[100:101], v[108:109]
	v_fmac_f64_e32 v[108:109], -2.0, v[106:107]
	v_cvt_f32_f64_e32 v110, v[104:105]
	v_cvt_f32_f64_e32 v111, v[108:109]
	v_cmp_gt_f32_e32 vcc, v110, v111
	s_nop 1
	s_and_b64 s[68:69], vcc, exec
	s_cselect_b32 s4, s64, s61
	s_branch .LBB0_148
.Lslowc_3:
	s_or_b32 s1, s29, 3
	s_lshl_b32 s5, s1, 2
	s_add_i32 s5, s5, 0x11100
	v_mov_b32_e32 v4, s5
	ds_read_b32 v4, v4
	s_mulk_i32 s1, 0x810
	v_add_u32_e32 v8, s1, v135
	s_waitcnt lgkmcnt(0)
	v_max_i32_e32 v4, 1, v4
	v_cvt_f64_u32_e32 v[12:13], v4
	v_div_scale_f64 v[14:15], s[26:27], v[12:13], v[12:13], 1.0
	v_rcp_f64_e32 v[16:17], v[14:15]
	v_div_scale_f64 v[20:21], vcc, 1.0, v[12:13], 1.0
	ds_read2st64_b64 v[4:7], v8 offset0:64 offset1:65
	ds_read2st64_b64 v[8:11], v8 offset0:66 offset1:67
	v_fma_f64 v[22:23], -v[14:15], v[16:17], 1.0
	v_fmac_f64_e32 v[16:17], v[16:17], v[22:23]
	v_fma_f64 v[22:23], -v[14:15], v[16:17], 1.0
	v_fmac_f64_e32 v[16:17], v[16:17], v[22:23]
	v_mul_f64 v[22:23], v[20:21], v[16:17]
	v_fma_f64 v[14:15], -v[14:15], v[22:23], v[20:21]
	v_div_fmas_f64 v[14:15], v[14:15], v[16:17], v[22:23]
	v_div_fixup_f64 v[12:13], v[14:15], v[12:13], 1.0
	s_waitcnt lgkmcnt(1)
	v_mul_f64 v[6:7], v[6:7], v[12:13]
	v_mul_f64 v[4:5], v[4:5], v[12:13]
	s_waitcnt lgkmcnt(0)
	v_mul_f64 v[8:9], v[8:9], v[12:13]
	v_mul_f64 v[10:11], v[12:13], v[10:11]
	v_mul_f64 v[12:13], v[6:7], v[6:7]
	v_fmac_f64_e32 v[12:13], v[4:5], v[4:5]
	v_fmac_f64_e32 v[12:13], v[8:9], v[8:9]
	v_fmac_f64_e32 v[12:13], v[10:11], v[10:11]
	s_nop 1
	v_mov_b32_dpp v14, v12 quad_perm:[1,0,3,2] row_mask:0xf bank_mask:0xf bound_ctrl:1
	v_mov_b32_dpp v15, v13 quad_perm:[1,0,3,2] row_mask:0xf bank_mask:0xf bound_ctrl:1
	v_add_f64 v[12:13], v[12:13], v[14:15]
	s_nop 1
	v_mov_b32_dpp v14, v12 quad_perm:[2,3,0,1] row_mask:0xf bank_mask:0xf bound_ctrl:1
	v_mov_b32_dpp v15, v13 quad_perm:[2,3,0,1] row_mask:0xf bank_mask:0xf bound_ctrl:1
	v_add_f64 v[12:13], v[12:13], v[14:15]
	s_nop 1
	v_mov_b32_dpp v14, v12 row_half_mirror row_mask:0xf bank_mask:0xf bound_ctrl:1
	v_mov_b32_dpp v15, v13 row_half_mirror row_mask:0xf bank_mask:0xf bound_ctrl:1
	v_add_f64 v[12:13], v[12:13], v[14:15]
	s_nop 1
	v_mov_b32_dpp v14, v12 row_mirror row_mask:0xf bank_mask:0xf bound_ctrl:1
	v_mov_b32_dpp v15, v13 row_mirror row_mask:0xf bank_mask:0xf bound_ctrl:1
	v_add_f64 v[12:13], v[12:13], v[14:15]
	s_nop 0
	v_readlane_b32 s1, v13, 16
	v_readlane_b32 s5, v12, 16
	v_readlane_b32 s27, v13, 0
	v_readlane_b32 s26, v12, 0
	v_mov_b32_e32 v14, s5
	v_mov_b32_e32 v15, s1
	v_readlane_b32 s1, v13, 48
	v_readlane_b32 s5, v12, 48
	v_add_f64 v[14:15], s[26:27], v[14:15]
	v_readlane_b32 s27, v13, 32
	v_readlane_b32 s26, v12, 32
	v_mov_b32_e32 v12, s5
	v_mov_b32_e32 v13, s1
	v_add_f64 v[12:13], s[26:27], v[12:13]
	v_add_f64 v[12:13], v[14:15], v[12:13]
	v_mov_b32_e32 v14, 0x7f800000
